# FFN-up next-unit row-index prefetch address simplified (one address, 4 offset loads), merge-GEMM mid-K hook loads issued together with one wait, RP2 activation loads issued before the router-weight LD
# speedup vs baseline: 1.0387x; 1.0034x over previous
.LBB0_579:
	s_cmp_lg_u32 s61, 8
	s_mov_b32 s66, 0x18000
	s_cbranch_scc1 .LBB0_581
	v_mov_b32_e32 v134, v0
	v_mov_b32_e32 v133, v195
	v_ashrrev_i32_e32 v130, 2, v134
	v_and_b32_e32 v130, 0xffffffc0, v130
	v_add_u32_e32 v130, s60, v130
	v_and_or_b32 v130, v134, 15, v130
	v_ashrrev_i32_e32 v131, 31, v130
	v_lshlrev_b64 v[130:131], 11, v[130:131]
	v_lshl_add_u64 v[130:131], s[20:21], 0, v[130:131]
	v_and_b32_e32 v132, 0xc0, v134
	v_lshl_add_u64 v[130:131], v[130:131], 0, v[132:133]
	v_and_b32_e32 v132, 48, v134
	v_lshl_add_u64 v[130:131], v[130:131], 0, v[132:133]
	s_mov_b32 s62, 0x8000
	global_load_dwordx4 v[182:185], v[130:131], off
	global_load_dwordx4 v[186:189], v[130:131], off offset:256
	v_add_co_u32_e32 v132, vcc, s62, v130
	s_nop 0
	s_nop 0
	v_addc_co_u32_e32 v133, vcc, 0, v131, vcc
	global_load_dwordx4 v[196:199], v[132:133], off
	global_load_dwordx4 v[178:181], v[132:133], off offset:256
	v_add_co_u32_e32 v132, vcc, s73, v130
	s_nop 0
	s_nop 0
	v_addc_co_u32_e32 v133, vcc, 0, v131, vcc
	global_load_dwordx4 v[174:177], v[132:133], off
	global_load_dwordx4 v[170:173], v[132:133], off offset:256
	v_add_co_u32_e32 v132, vcc, s66, v130
	s_nop 0
	s_nop 0
	v_addc_co_u32_e32 v133, vcc, 0, v131, vcc
	global_load_dwordx4 v[166:169], v[132:133], off
	global_load_dwordx4 v[162:165], v[132:133], off offset:256
	v_add_co_u32_e32 v132, vcc, s88, v130
	s_nop 0
	s_nop 0
	v_addc_co_u32_e32 v133, vcc, 0, v131, vcc
	global_load_dwordx4 v[158:161], v[132:133], off
	global_load_dwordx4 v[154:157], v[132:133], off offset:256
	v_add_co_u32_e32 v132, vcc, s94, v130
	s_nop 0
	s_nop 0
	v_addc_co_u32_e32 v133, vcc, 0, v131, vcc
	global_load_dwordx4 v[150:153], v[132:133], off
	global_load_dwordx4 v[146:149], v[132:133], off offset:256
	v_add_co_u32_e32 v132, vcc, s89, v130
	s_nop 0
	s_nop 0
	v_addc_co_u32_e32 v133, vcc, 0, v131, vcc
	global_load_dwordx4 v[142:145], v[132:133], off
	global_load_dwordx4 v[134:137], v[132:133], off offset:256
	v_add_co_u32_e32 v130, vcc, s95, v130
	s_nop 0
	s_nop 0
	v_addc_co_u32_e32 v131, vcc, 0, v131, vcc
	global_load_dwordx4 v[138:141], v[130:131], off
	s_nop 0
	global_load_dwordx4 v[130:133], v[130:131], off offset:256
	s_waitcnt vmcnt(0)
	v_lshlrev_b32_e32 v200, 16, v182
	v_and_b32_e32 v201, 0xffff0000, v182
	v_lshlrev_b32_e32 v182, 16, v183
	v_and_b32_e32 v183, 0xffff0000, v183
	v_lshlrev_b32_e32 v202, 16, v184
	v_and_b32_e32 v203, 0xffff0000, v184
	v_lshlrev_b32_e32 v184, 16, v185
	v_and_b32_e32 v185, 0xffff0000, v185
	v_pk_mul_f32 v[124:125], v[124:125], v[182:183]
	v_pk_mul_f32 v[128:129], v[128:129], v[184:185]
	v_lshlrev_b32_e32 v182, 16, v186
	v_and_b32_e32 v183, 0xffff0000, v186
	v_lshlrev_b32_e32 v184, 16, v187
	v_and_b32_e32 v185, 0xffff0000, v187
	v_pk_mul_f32 v[120:121], v[120:121], v[184:185]
	v_pk_mul_f32 v[118:119], v[118:119], v[182:183]
	v_lshlrev_b32_e32 v186, 16, v188
	v_and_b32_e32 v187, 0xffff0000, v188
	v_lshlrev_b32_e32 v188, 16, v189
	v_and_b32_e32 v189, 0xffff0000, v189
	v_pk_mul_f32 v[116:117], v[116:117], v[188:189]
	v_pk_mul_f32 v[114:115], v[114:115], v[186:187]
	v_pk_mul_f32 v[122:123], v[122:123], v[200:201]
	v_pk_mul_f32 v[126:127], v[126:127], v[202:203]
	s_waitcnt vmcnt(0)
	v_lshlrev_b32_e32 v182, 16, v196
	v_and_b32_e32 v183, 0xffff0000, v196
	v_lshlrev_b32_e32 v184, 16, v197
	v_and_b32_e32 v185, 0xffff0000, v197
	v_pk_mul_f32 v[112:113], v[112:113], v[184:185]
	v_pk_mul_f32 v[110:111], v[110:111], v[182:183]
	v_lshlrev_b32_e32 v182, 16, v178
	v_and_b32_e32 v183, 0xffff0000, v178
	v_lshlrev_b32_e32 v178, 16, v179
	v_and_b32_e32 v179, 0xffff0000, v179
	v_lshlrev_b32_e32 v184, 16, v180
	v_and_b32_e32 v185, 0xffff0000, v180
	v_lshlrev_b32_e32 v180, 16, v181
	v_and_b32_e32 v181, 0xffff0000, v181
	v_pk_mul_f32 v[104:105], v[104:105], v[178:179]
	v_pk_mul_f32 v[100:101], v[100:101], v[180:181]
	v_lshlrev_b32_e32 v178, 16, v174
	v_and_b32_e32 v179, 0xffff0000, v174
	v_lshlrev_b32_e32 v174, 16, v175
	v_and_b32_e32 v175, 0xffff0000, v175
	v_lshlrev_b32_e32 v180, 16, v176
	v_and_b32_e32 v181, 0xffff0000, v176
	v_lshlrev_b32_e32 v176, 16, v177
	v_and_b32_e32 v177, 0xffff0000, v177
	v_pk_mul_f32 v[96:97], v[96:97], v[174:175]
	v_pk_mul_f32 v[92:93], v[92:93], v[176:177]
	v_lshlrev_b32_e32 v174, 16, v170
	v_and_b32_e32 v175, 0xffff0000, v170
	v_lshlrev_b32_e32 v170, 16, v171
	v_and_b32_e32 v171, 0xffff0000, v171
	v_lshlrev_b32_e32 v176, 16, v172
	v_and_b32_e32 v177, 0xffff0000, v172
	v_lshlrev_b32_e32 v172, 16, v173
	v_and_b32_e32 v173, 0xffff0000, v173
	v_pk_mul_f32 v[88:89], v[88:89], v[170:171]
	v_pk_mul_f32 v[84:85], v[84:85], v[172:173]
	v_lshlrev_b32_e32 v170, 16, v166
	v_and_b32_e32 v171, 0xffff0000, v166
	v_lshlrev_b32_e32 v166, 16, v167
	v_and_b32_e32 v167, 0xffff0000, v167
	v_lshlrev_b32_e32 v172, 16, v168
	v_and_b32_e32 v173, 0xffff0000, v168
	v_lshlrev_b32_e32 v168, 16, v169
	v_and_b32_e32 v169, 0xffff0000, v169
	v_pk_mul_f32 v[80:81], v[80:81], v[166:167]
	v_pk_mul_f32 v[76:77], v[76:77], v[168:169]
	v_lshlrev_b32_e32 v166, 16, v162
	v_and_b32_e32 v167, 0xffff0000, v162
	v_lshlrev_b32_e32 v162, 16, v163
	v_and_b32_e32 v163, 0xffff0000, v163
	v_lshlrev_b32_e32 v168, 16, v164
	v_and_b32_e32 v169, 0xffff0000, v164
	v_lshlrev_b32_e32 v164, 16, v165
	v_and_b32_e32 v165, 0xffff0000, v165
	v_pk_mul_f32 v[72:73], v[72:73], v[162:163]
	v_pk_mul_f32 v[68:69], v[68:69], v[164:165]
	v_lshlrev_b32_e32 v162, 16, v158
	v_and_b32_e32 v163, 0xffff0000, v158
	v_lshlrev_b32_e32 v158, 16, v159
	v_and_b32_e32 v159, 0xffff0000, v159
	v_lshlrev_b32_e32 v164, 16, v160
	v_and_b32_e32 v165, 0xffff0000, v160
	v_lshlrev_b32_e32 v160, 16, v161
	v_and_b32_e32 v161, 0xffff0000, v161
	v_pk_mul_f32 v[64:65], v[64:65], v[158:159]
	v_pk_mul_f32 v[60:61], v[60:61], v[160:161]
	v_lshlrev_b32_e32 v158, 16, v154
	v_and_b32_e32 v159, 0xffff0000, v154
	v_lshlrev_b32_e32 v154, 16, v155
	v_and_b32_e32 v155, 0xffff0000, v155
	v_lshlrev_b32_e32 v160, 16, v156
	v_and_b32_e32 v161, 0xffff0000, v156
	v_lshlrev_b32_e32 v156, 16, v157
	v_and_b32_e32 v157, 0xffff0000, v157
	v_pk_mul_f32 v[56:57], v[56:57], v[154:155]
	v_pk_mul_f32 v[52:53], v[52:53], v[156:157]
	v_lshlrev_b32_e32 v154, 16, v150
	v_and_b32_e32 v155, 0xffff0000, v150
	v_lshlrev_b32_e32 v150, 16, v151
	v_and_b32_e32 v151, 0xffff0000, v151
	v_lshlrev_b32_e32 v156, 16, v152
	v_and_b32_e32 v157, 0xffff0000, v152
	v_lshlrev_b32_e32 v152, 16, v153
	v_and_b32_e32 v153, 0xffff0000, v153
	v_pk_mul_f32 v[48:49], v[48:49], v[150:151]
	v_pk_mul_f32 v[44:45], v[44:45], v[152:153]
	v_lshlrev_b32_e32 v150, 16, v146
	v_and_b32_e32 v151, 0xffff0000, v146
	v_lshlrev_b32_e32 v146, 16, v147
	v_and_b32_e32 v147, 0xffff0000, v147
	v_lshlrev_b32_e32 v152, 16, v148
	v_and_b32_e32 v153, 0xffff0000, v148
	v_lshlrev_b32_e32 v148, 16, v149
	v_and_b32_e32 v149, 0xffff0000, v149
	v_pk_mul_f32 v[40:41], v[40:41], v[146:147]
	v_pk_mul_f32 v[36:37], v[36:37], v[148:149]
	v_lshlrev_b32_e32 v146, 16, v142
	v_and_b32_e32 v147, 0xffff0000, v142
	v_lshlrev_b32_e32 v142, 16, v143
	v_and_b32_e32 v143, 0xffff0000, v143
	v_lshlrev_b32_e32 v148, 16, v144
	v_and_b32_e32 v149, 0xffff0000, v144
	v_lshlrev_b32_e32 v144, 16, v145
	v_and_b32_e32 v145, 0xffff0000, v145
	v_pk_mul_f32 v[32:33], v[32:33], v[142:143]
	v_pk_mul_f32 v[28:29], v[28:29], v[144:145]
	v_lshlrev_b32_e32 v142, 16, v134
	v_and_b32_e32 v143, 0xffff0000, v134
	v_lshlrev_b32_e32 v134, 16, v135
	v_and_b32_e32 v135, 0xffff0000, v135
	v_lshlrev_b32_e32 v144, 16, v136
	v_and_b32_e32 v145, 0xffff0000, v136
	v_lshlrev_b32_e32 v136, 16, v137
	v_and_b32_e32 v137, 0xffff0000, v137
	v_pk_mul_f32 v[24:25], v[24:25], v[134:135]
	v_pk_mul_f32 v[20:21], v[20:21], v[136:137]
	v_lshlrev_b32_e32 v134, 16, v138
	v_and_b32_e32 v135, 0xffff0000, v138
	v_lshlrev_b32_e32 v136, 16, v139
	v_and_b32_e32 v137, 0xffff0000, v139
	v_lshlrev_b32_e32 v186, 16, v198
	v_and_b32_e32 v187, 0xffff0000, v198
	v_lshlrev_b32_e32 v188, 16, v199
	v_and_b32_e32 v189, 0xffff0000, v199
	v_lshlrev_b32_e32 v138, 16, v140
	v_and_b32_e32 v139, 0xffff0000, v140
	v_lshlrev_b32_e32 v140, 16, v141
	v_and_b32_e32 v141, 0xffff0000, v141
	v_pk_mul_f32 v[16:17], v[16:17], v[136:137]
	v_pk_mul_f32 v[14:15], v[14:15], v[134:135]
	v_lshlrev_b32_e32 v134, 16, v130
	v_and_b32_e32 v135, 0xffff0000, v130
	v_lshlrev_b32_e32 v130, 16, v131
	v_and_b32_e32 v131, 0xffff0000, v131
	v_lshlrev_b32_e32 v136, 16, v132
	v_and_b32_e32 v137, 0xffff0000, v132
	v_lshlrev_b32_e32 v132, 16, v133
	v_and_b32_e32 v133, 0xffff0000, v133
	v_pk_mul_f32 v[108:109], v[108:109], v[188:189]
	v_pk_mul_f32 v[106:107], v[106:107], v[186:187]
	v_pk_mul_f32 v[102:103], v[102:103], v[182:183]
	v_pk_mul_f32 v[98:99], v[98:99], v[184:185]
	v_pk_mul_f32 v[94:95], v[94:95], v[178:179]
	v_pk_mul_f32 v[90:91], v[90:91], v[180:181]
	v_pk_mul_f32 v[86:87], v[86:87], v[174:175]
	v_pk_mul_f32 v[82:83], v[82:83], v[176:177]
	v_pk_mul_f32 v[78:79], v[78:79], v[170:171]
	v_pk_mul_f32 v[74:75], v[74:75], v[172:173]
	v_pk_mul_f32 v[70:71], v[70:71], v[166:167]
	v_pk_mul_f32 v[66:67], v[66:67], v[168:169]
	v_pk_mul_f32 v[62:63], v[62:63], v[162:163]
	v_pk_mul_f32 v[58:59], v[58:59], v[164:165]
	v_pk_mul_f32 v[54:55], v[54:55], v[158:159]
	v_pk_mul_f32 v[50:51], v[50:51], v[160:161]
	v_pk_mul_f32 v[46:47], v[46:47], v[154:155]
	v_pk_mul_f32 v[42:43], v[42:43], v[156:157]
	v_pk_mul_f32 v[38:39], v[38:39], v[150:151]
	v_pk_mul_f32 v[34:35], v[34:35], v[152:153]
	v_pk_mul_f32 v[30:31], v[30:31], v[146:147]
	v_pk_mul_f32 v[26:27], v[26:27], v[148:149]
	v_pk_mul_f32 v[22:23], v[22:23], v[142:143]
	v_pk_mul_f32 v[18:19], v[18:19], v[144:145]
	v_pk_mul_f32 v[12:13], v[12:13], v[140:141]
	v_pk_mul_f32 v[10:11], v[10:11], v[138:139]
	v_pk_mul_f32 v[8:9], v[8:9], v[130:131]
	v_pk_mul_f32 v[6:7], v[6:7], v[134:135]
	v_pk_mul_f32 v[4:5], v[4:5], v[132:133]
	v_pk_mul_f32 v[2:3], v[2:3], v[136:137]

.LBB0_729:
	v_readlane_b32 s12, v253, 40
	v_readlane_b32 s13, v253, 41
	v_readlane_b32 s14, v253, 42
	v_readlane_b32 s15, v253, 43
	v_readlane_b32 s16, v253, 44
	v_readlane_b32 s17, v253, 45
	v_readlane_b32 s18, v253, 46
	v_readlane_b32 s19, v253, 47
	v_readlane_b32 s20, v253, 48
	v_readlane_b32 s21, v253, 49
	v_readlane_b32 s22, v253, 50
	v_readlane_b32 s23, v253, 51
	v_readlane_b32 s24, v253, 52
	v_readlane_b32 s25, v253, 53
	v_readlane_b32 s26, v253, 54
	v_readlane_b32 s27, v253, 55
	s_mov_b64 s[12:13], s[16:17]
	s_lshl_b32 s62, s36, 14
	s_mov_b64 s[14:15], s[18:19]
	s_mov_b64 s[16:17], s[20:21]
	s_mov_b64 s[18:19], s[22:23]
	s_mov_b64 s[20:21], s[24:25]
	s_mov_b64 s[22:23], s[26:27]
	s_add_u32 s0, s22, s0
	s_addc_u32 s1, s23, s1
	s_mov_b32 s101, 0
	s_cmpk_lg_i32 s10, 0x100
	s_cbranch_scc1 .Lrp2_nohoist
	s_lshl_b32 s4, s11, 7
	v_readlane_b32 s5, v254, 54
	s_add_i32 s4, s4, s5
	v_and_b32_e32 v200, 15, v32
	v_bfe_u32 v202, v32, 4, 2
	v_add_u32_e32 v200, s4, v200
	v_mov_b32_e32 v201, 0
	v_lshlrev_b32_e32 v202, 4, v202
	v_mov_b32_e32 v203, 0
	v_lshlrev_b64 v[200:201], 11, v[200:201]
	s_mov_b64 s[4:5], 0x4a000000
	v_lshl_add_u64 v[200:201], v[200:201], 0, v[202:203]
	v_lshl_add_u64 v[200:201], v[200:201], 0, s[0:1]
	v_lshl_add_u64 v[200:201], v[200:201], 0, s[4:5]
	global_load_dwordx4 v[130:133], v[200:201], off
	global_load_dwordx4 v[126:129], v[200:201], off offset:64
	global_load_dwordx4 v[122:125], v[200:201], off offset:128
	global_load_dwordx4 v[118:121], v[200:201], off offset:192
	global_load_dwordx4 v[114:117], v[200:201], off offset:256
	global_load_dwordx4 v[110:113], v[200:201], off offset:320
	global_load_dwordx4 v[106:109], v[200:201], off offset:384
	global_load_dwordx4 v[102:105], v[200:201], off offset:448
	global_load_dwordx4 v[98:101], v[200:201], off offset:512
	global_load_dwordx4 v[94:97], v[200:201], off offset:576
	global_load_dwordx4 v[90:93], v[200:201], off offset:640
	global_load_dwordx4 v[86:89], v[200:201], off offset:704
	global_load_dwordx4 v[82:85], v[200:201], off offset:768
	global_load_dwordx4 v[78:81], v[200:201], off offset:832
	global_load_dwordx4 v[74:77], v[200:201], off offset:896
	global_load_dwordx4 v[70:73], v[200:201], off offset:960
	global_load_dwordx4 v[66:69], v[200:201], off offset:1024
	global_load_dwordx4 v[62:65], v[200:201], off offset:1088
	global_load_dwordx4 v[58:61], v[200:201], off offset:1152
	global_load_dwordx4 v[54:57], v[200:201], off offset:1216
	global_load_dwordx4 v[50:53], v[200:201], off offset:1280
	global_load_dwordx4 v[46:49], v[200:201], off offset:1344
	s_mov_b32 s101, 1
.Lrp2_nohoist:
	s_lshl_b64 s[2:3], s[62:63], 2
	s_add_u32 s2, s0, s2
	v_lshlrev_b32_e32 v30, 2, v32
	s_addc_u32 s3, s1, s3
	v_ashrrev_i32_e32 v31, 31, v30
	v_lshl_add_u64 v[2:3], v[30:31], 2, s[2:3]
	s_mov_b32 s2, 0x150000
	v_add_co_u32_e32 v4, vcc, s2, v2
	s_mov_b32 s2, 0x152000
	s_nop 0
	v_addc_co_u32_e32 v5, vcc, 0, v3, vcc
	global_load_dwordx4 v[34:37], v[4:5], off
	v_add_co_u32_e32 v4, vcc, s2, v2
	s_mov_b32 s2, 0x154000
	s_nop 0
	v_addc_co_u32_e32 v5, vcc, 0, v3, vcc
	global_load_dwordx4 v[26:29], v[4:5], off
	v_add_co_u32_e32 v4, vcc, s2, v2
	s_mov_b32 s2, 0x156000
	s_nop 0
	v_addc_co_u32_e32 v5, vcc, 0, v3, vcc
	global_load_dwordx4 v[22:25], v[4:5], off
	v_add_co_u32_e32 v4, vcc, s2, v2
	s_mov_b32 s2, 0x158000
	s_nop 0
	v_addc_co_u32_e32 v5, vcc, 0, v3, vcc
	global_load_dwordx4 v[18:21], v[4:5], off
	v_add_co_u32_e32 v4, vcc, s2, v2
	s_mov_b32 s2, 0x15a000
	s_nop 0
	v_addc_co_u32_e32 v5, vcc, 0, v3, vcc
	global_load_dwordx4 v[14:17], v[4:5], off
	v_add_co_u32_e32 v4, vcc, s2, v2
	s_mov_b32 s2, 0x15c000
	s_nop 0
	v_addc_co_u32_e32 v5, vcc, 0, v3, vcc
	global_load_dwordx4 v[10:13], v[4:5], off
	v_add_co_u32_e32 v4, vcc, s2, v2
	v_lshrrev_b32_e32 v31, 8, v32
	s_nop 0
	v_addc_co_u32_e32 v5, vcc, 0, v3, vcc
	global_load_dwordx4 v[6:9], v[4:5], off
	v_mul_i32_i24_e32 v31, 0x408, v31
	s_mov_b32 s2, 0x15e000
	v_add_co_u32_e32 v2, vcc, s2, v2
	s_lshl_b32 s2, s11, 3
	s_nop 0
	v_addc_co_u32_e32 v3, vcc, 0, v3, vcc
	global_load_dwordx4 v[2:5], v[2:3], off
	v_readlane_b32 s3, v253, 29
	s_add_i32 s6, s2, s3
	s_cmpk_gt_i32 s6, 0x7ff
	s_mov_b32 s12, 0xc2ce8ed0
	s_mov_b32 s13, 0x42b17218
	s_waitcnt vmcnt(7)
	v_and_b32_sdwa v33, v36, v237 dst_sel:DWORD dst_unused:UNUSED_PAD src0_sel:WORD_1 src1_sel:DWORD
	v_and_b32_sdwa v40, v34, v237 dst_sel:DWORD dst_unused:UNUSED_PAD src0_sel:WORD_1 src1_sel:DWORD
	v_add3_u32 v33, v36, v33, s65
	v_add3_u32 v42, v34, v40, s65
	v_mov_b32_e32 v38, v34
	v_mov_b32_e32 v39, v36
	v_and_b32_e32 v41, 0xffff0000, v33
	v_and_b32_e32 v40, 0xffff0000, v42
	v_pk_add_f32 v[38:39], v[38:39], v[40:41] neg_lo:[0,1] neg_hi:[0,1]
	v_and_b32_sdwa v40, v35, v237 dst_sel:DWORD dst_unused:UNUSED_PAD src0_sel:WORD_1 src1_sel:DWORD
	v_and_b32_sdwa v34, v39, v237 dst_sel:DWORD dst_unused:UNUSED_PAD src0_sel:WORD_1 src1_sel:DWORD
	v_add3_u32 v39, v39, v34, s65
	v_and_b32_sdwa v34, v37, v237 dst_sel:DWORD dst_unused:UNUSED_PAD src0_sel:WORD_1 src1_sel:DWORD
	v_and_b32_sdwa v36, v38, v237 dst_sel:DWORD dst_unused:UNUSED_PAD src0_sel:WORD_1 src1_sel:DWORD
	v_add3_u32 v34, v37, v34, s65
	v_add3_u32 v40, v35, v40, s65
	v_add3_u32 v38, v38, v36, s65
	v_mov_b32_e32 v36, v35
	v_and_b32_e32 v35, 0xffff0000, v34
	v_and_b32_e32 v34, 0xffff0000, v40
	v_pk_add_f32 v[36:37], v[36:37], v[34:35] neg_lo:[0,1] neg_hi:[0,1]
	v_or_b32_sdwa v35, v35, v33 dst_sel:DWORD dst_unused:UNUSED_PAD src0_sel:DWORD src1_sel:WORD_1
	v_and_b32_sdwa v40, v37, v237 dst_sel:DWORD dst_unused:UNUSED_PAD src0_sel:WORD_1 src1_sel:DWORD
	v_and_b32_sdwa v41, v36, v237 dst_sel:DWORD dst_unused:UNUSED_PAD src0_sel:WORD_1 src1_sel:DWORD
	v_add3_u32 v37, v37, v40, s65
	v_add3_u32 v36, v36, v41, s65
	v_lshlrev_b32_e32 v33, 1, v31
	v_lshlrev_b32_e32 v31, 3, v32
	v_and_b32_e32 v37, 0xffff0000, v37
	v_and_b32_e32 v36, 0xffff0000, v36
	v_and_b32_e32 v31, 0x7f8, v31
	v_or_b32_sdwa v34, v34, v42 dst_sel:DWORD dst_unused:UNUSED_PAD src0_sel:DWORD src1_sel:WORD_1
	v_or_b32_sdwa v37, v37, v39 dst_sel:DWORD dst_unused:UNUSED_PAD src0_sel:DWORD src1_sel:WORD_1
	v_or_b32_sdwa v36, v36, v38 dst_sel:DWORD dst_unused:UNUSED_PAD src0_sel:DWORD src1_sel:WORD_1
	v_add3_u32 v33, 0, v33, v31
	ds_write_b64 v33, v[34:35]
	ds_write_b64 v33, v[36:37] offset:33024
	s_waitcnt vmcnt(6)
	v_and_b32_sdwa v36, v28, v237 dst_sel:DWORD dst_unused:UNUSED_PAD src0_sel:WORD_1 src1_sel:DWORD
	v_and_b32_sdwa v37, v26, v237 dst_sel:DWORD dst_unused:UNUSED_PAD src0_sel:WORD_1 src1_sel:DWORD
	v_add3_u32 v38, v28, v36, s65
	v_add3_u32 v39, v26, v37, s65
	v_mov_b32_e32 v34, v26
	v_mov_b32_e32 v35, v28
	v_and_b32_e32 v37, 0xffff0000, v38
	v_and_b32_e32 v36, 0xffff0000, v39
	v_pk_add_f32 v[34:35], v[34:35], v[36:37] neg_lo:[0,1] neg_hi:[0,1]
	v_and_b32_sdwa v36, v27, v237 dst_sel:DWORD dst_unused:UNUSED_PAD src0_sel:WORD_1 src1_sel:DWORD
	v_and_b32_sdwa v26, v35, v237 dst_sel:DWORD dst_unused:UNUSED_PAD src0_sel:WORD_1 src1_sel:DWORD
	v_add3_u32 v35, v35, v26, s65
	v_and_b32_sdwa v26, v29, v237 dst_sel:DWORD dst_unused:UNUSED_PAD src0_sel:WORD_1 src1_sel:DWORD
	v_and_b32_sdwa v28, v34, v237 dst_sel:DWORD dst_unused:UNUSED_PAD src0_sel:WORD_1 src1_sel:DWORD
	v_add3_u32 v26, v29, v26, s65
	v_add3_u32 v36, v27, v36, s65
	v_add3_u32 v34, v34, v28, s65
	v_mov_b32_e32 v28, v27
	v_and_b32_e32 v27, 0xffff0000, v26
	v_and_b32_e32 v26, 0xffff0000, v36
	v_add_u32_e32 v33, 0x800, v30
	v_pk_add_f32 v[28:29], v[28:29], v[26:27] neg_lo:[0,1] neg_hi:[0,1]
	v_ashrrev_i32_e32 v33, 10, v33
	v_and_b32_sdwa v36, v29, v237 dst_sel:DWORD dst_unused:UNUSED_PAD src0_sel:WORD_1 src1_sel:DWORD
	v_and_b32_sdwa v37, v28, v237 dst_sel:DWORD dst_unused:UNUSED_PAD src0_sel:WORD_1 src1_sel:DWORD
	v_add3_u32 v29, v29, v36, s65
	v_add3_u32 v28, v28, v37, s65
	v_mul_i32_i24_e32 v33, 0x408, v33
	v_and_b32_e32 v29, 0xffff0000, v29
	v_and_b32_e32 v28, 0xffff0000, v28
	v_lshlrev_b32_e32 v33, 1, v33
	v_or_b32_sdwa v26, v26, v39 dst_sel:DWORD dst_unused:UNUSED_PAD src0_sel:DWORD src1_sel:WORD_1
	v_or_b32_sdwa v27, v27, v38 dst_sel:DWORD dst_unused:UNUSED_PAD src0_sel:DWORD src1_sel:WORD_1
	v_or_b32_sdwa v29, v29, v35 dst_sel:DWORD dst_unused:UNUSED_PAD src0_sel:DWORD src1_sel:WORD_1
	v_or_b32_sdwa v28, v28, v34 dst_sel:DWORD dst_unused:UNUSED_PAD src0_sel:DWORD src1_sel:WORD_1
	v_add3_u32 v33, 0, v33, v31
	ds_write_b64 v33, v[26:27]
	ds_write_b64 v33, v[28:29] offset:33024
	s_waitcnt vmcnt(5)
	v_and_b32_sdwa v28, v24, v237 dst_sel:DWORD dst_unused:UNUSED_PAD src0_sel:WORD_1 src1_sel:DWORD
	v_and_b32_sdwa v29, v22, v237 dst_sel:DWORD dst_unused:UNUSED_PAD src0_sel:WORD_1 src1_sel:DWORD
	v_add_u32_e32 v26, 0x1000, v30
	v_add3_u32 v34, v24, v28, s65
	v_add3_u32 v35, v22, v29, s65
	v_ashrrev_i32_e32 v33, 10, v26
	v_mov_b32_e32 v26, v22
	v_mov_b32_e32 v27, v24
	v_and_b32_e32 v29, 0xffff0000, v34
	v_and_b32_e32 v28, 0xffff0000, v35
	v_pk_add_f32 v[26:27], v[26:27], v[28:29] neg_lo:[0,1] neg_hi:[0,1]
	v_and_b32_sdwa v28, v23, v237 dst_sel:DWORD dst_unused:UNUSED_PAD src0_sel:WORD_1 src1_sel:DWORD
	v_and_b32_sdwa v22, v27, v237 dst_sel:DWORD dst_unused:UNUSED_PAD src0_sel:WORD_1 src1_sel:DWORD
	v_add3_u32 v27, v27, v22, s65
	v_and_b32_sdwa v22, v25, v237 dst_sel:DWORD dst_unused:UNUSED_PAD src0_sel:WORD_1 src1_sel:DWORD
	v_and_b32_sdwa v24, v26, v237 dst_sel:DWORD dst_unused:UNUSED_PAD src0_sel:WORD_1 src1_sel:DWORD
	v_add3_u32 v22, v25, v22, s65
	v_add3_u32 v28, v23, v28, s65
	v_add3_u32 v26, v26, v24, s65
	v_mov_b32_e32 v24, v23
	v_and_b32_e32 v23, 0xffff0000, v22
	v_and_b32_e32 v22, 0xffff0000, v28
	v_pk_add_f32 v[24:25], v[24:25], v[22:23] neg_lo:[0,1] neg_hi:[0,1]
	v_or_b32_sdwa v22, v22, v35 dst_sel:DWORD dst_unused:UNUSED_PAD src0_sel:DWORD src1_sel:WORD_1
	v_and_b32_sdwa v29, v24, v237 dst_sel:DWORD dst_unused:UNUSED_PAD src0_sel:WORD_1 src1_sel:DWORD
	v_add3_u32 v24, v24, v29, s65
	v_and_b32_sdwa v28, v25, v237 dst_sel:DWORD dst_unused:UNUSED_PAD src0_sel:WORD_1 src1_sel:DWORD
	v_and_b32_e32 v24, 0xffff0000, v24
	v_add3_u32 v25, v25, v28, s65
	v_or_b32_sdwa v24, v24, v26 dst_sel:DWORD dst_unused:UNUSED_PAD src0_sel:DWORD src1_sel:WORD_1
	v_mul_i32_i24_e32 v26, 0x408, v33
	v_and_b32_e32 v25, 0xffff0000, v25
	v_lshlrev_b32_e32 v26, 1, v26
	v_or_b32_sdwa v23, v23, v34 dst_sel:DWORD dst_unused:UNUSED_PAD src0_sel:DWORD src1_sel:WORD_1
	v_or_b32_sdwa v25, v25, v27 dst_sel:DWORD dst_unused:UNUSED_PAD src0_sel:DWORD src1_sel:WORD_1
	v_add3_u32 v26, 0, v26, v31
	ds_write_b64 v26, v[22:23]
	ds_write_b64 v26, v[24:25] offset:33024
	s_waitcnt vmcnt(4)
	v_and_b32_sdwa v24, v20, v237 dst_sel:DWORD dst_unused:UNUSED_PAD src0_sel:WORD_1 src1_sel:DWORD
	v_and_b32_sdwa v25, v18, v237 dst_sel:DWORD dst_unused:UNUSED_PAD src0_sel:WORD_1 src1_sel:DWORD
	v_add_u32_e32 v22, 0x1800, v30
	v_add3_u32 v27, v20, v24, s65
	v_add3_u32 v28, v18, v25, s65
	v_ashrrev_i32_e32 v26, 10, v22
	v_mov_b32_e32 v22, v18
	v_mov_b32_e32 v23, v20
	v_and_b32_e32 v25, 0xffff0000, v27
	v_and_b32_e32 v24, 0xffff0000, v28
	v_pk_add_f32 v[22:23], v[22:23], v[24:25] neg_lo:[0,1] neg_hi:[0,1]
	v_and_b32_sdwa v24, v19, v237 dst_sel:DWORD dst_unused:UNUSED_PAD src0_sel:WORD_1 src1_sel:DWORD
	v_and_b32_sdwa v18, v23, v237 dst_sel:DWORD dst_unused:UNUSED_PAD src0_sel:WORD_1 src1_sel:DWORD
	v_add3_u32 v23, v23, v18, s65
	v_and_b32_sdwa v18, v21, v237 dst_sel:DWORD dst_unused:UNUSED_PAD src0_sel:WORD_1 src1_sel:DWORD
	v_and_b32_sdwa v20, v22, v237 dst_sel:DWORD dst_unused:UNUSED_PAD src0_sel:WORD_1 src1_sel:DWORD
	v_add3_u32 v18, v21, v18, s65
	v_add3_u32 v24, v19, v24, s65
	v_add3_u32 v22, v22, v20, s65
	v_mov_b32_e32 v20, v19
	v_and_b32_e32 v19, 0xffff0000, v18
	v_and_b32_e32 v18, 0xffff0000, v24
	v_pk_add_f32 v[20:21], v[20:21], v[18:19] neg_lo:[0,1] neg_hi:[0,1]
	v_or_b32_sdwa v18, v18, v28 dst_sel:DWORD dst_unused:UNUSED_PAD src0_sel:DWORD src1_sel:WORD_1
	v_and_b32_sdwa v25, v20, v237 dst_sel:DWORD dst_unused:UNUSED_PAD src0_sel:WORD_1 src1_sel:DWORD
	v_add3_u32 v20, v20, v25, s65
	v_and_b32_sdwa v24, v21, v237 dst_sel:DWORD dst_unused:UNUSED_PAD src0_sel:WORD_1 src1_sel:DWORD
	v_and_b32_e32 v20, 0xffff0000, v20
	v_add3_u32 v21, v21, v24, s65
	v_or_b32_sdwa v20, v20, v22 dst_sel:DWORD dst_unused:UNUSED_PAD src0_sel:DWORD src1_sel:WORD_1
	v_mul_i32_i24_e32 v22, 0x408, v26
	v_and_b32_e32 v21, 0xffff0000, v21
	v_lshlrev_b32_e32 v22, 1, v22
	v_or_b32_sdwa v19, v19, v27 dst_sel:DWORD dst_unused:UNUSED_PAD src0_sel:DWORD src1_sel:WORD_1
	v_or_b32_sdwa v21, v21, v23 dst_sel:DWORD dst_unused:UNUSED_PAD src0_sel:DWORD src1_sel:WORD_1
	v_add3_u32 v22, 0, v22, v31
	ds_write_b64 v22, v[18:19]
	ds_write_b64 v22, v[20:21] offset:33024
	s_waitcnt vmcnt(3)
	v_and_b32_sdwa v20, v16, v237 dst_sel:DWORD dst_unused:UNUSED_PAD src0_sel:WORD_1 src1_sel:DWORD
	v_and_b32_sdwa v21, v14, v237 dst_sel:DWORD dst_unused:UNUSED_PAD src0_sel:WORD_1 src1_sel:DWORD
	v_add_u32_e32 v18, 0x2000, v30
	v_add3_u32 v23, v16, v20, s65
	v_add3_u32 v24, v14, v21, s65
	v_ashrrev_i32_e32 v22, 10, v18
	v_mov_b32_e32 v18, v14
	v_mov_b32_e32 v19, v16
	v_and_b32_e32 v21, 0xffff0000, v23
	v_and_b32_e32 v20, 0xffff0000, v24
	v_pk_add_f32 v[18:19], v[18:19], v[20:21] neg_lo:[0,1] neg_hi:[0,1]
	v_and_b32_sdwa v20, v15, v237 dst_sel:DWORD dst_unused:UNUSED_PAD src0_sel:WORD_1 src1_sel:DWORD
	v_and_b32_sdwa v14, v19, v237 dst_sel:DWORD dst_unused:UNUSED_PAD src0_sel:WORD_1 src1_sel:DWORD
	v_add3_u32 v19, v19, v14, s65
	v_and_b32_sdwa v14, v17, v237 dst_sel:DWORD dst_unused:UNUSED_PAD src0_sel:WORD_1 src1_sel:DWORD
	v_and_b32_sdwa v16, v18, v237 dst_sel:DWORD dst_unused:UNUSED_PAD src0_sel:WORD_1 src1_sel:DWORD
	v_add3_u32 v14, v17, v14, s65
	v_add3_u32 v20, v15, v20, s65
	v_add3_u32 v18, v18, v16, s65
	v_mov_b32_e32 v16, v15
	v_and_b32_e32 v15, 0xffff0000, v14
	v_and_b32_e32 v14, 0xffff0000, v20
	v_pk_add_f32 v[16:17], v[16:17], v[14:15] neg_lo:[0,1] neg_hi:[0,1]
	v_or_b32_sdwa v14, v14, v24 dst_sel:DWORD dst_unused:UNUSED_PAD src0_sel:DWORD src1_sel:WORD_1
	v_and_b32_sdwa v21, v16, v237 dst_sel:DWORD dst_unused:UNUSED_PAD src0_sel:WORD_1 src1_sel:DWORD
	v_add3_u32 v16, v16, v21, s65
	v_and_b32_sdwa v20, v17, v237 dst_sel:DWORD dst_unused:UNUSED_PAD src0_sel:WORD_1 src1_sel:DWORD
	v_and_b32_e32 v16, 0xffff0000, v16
	v_add3_u32 v17, v17, v20, s65
	v_or_b32_sdwa v16, v16, v18 dst_sel:DWORD dst_unused:UNUSED_PAD src0_sel:DWORD src1_sel:WORD_1
	v_mul_i32_i24_e32 v18, 0x408, v22
	v_and_b32_e32 v17, 0xffff0000, v17
	v_lshlrev_b32_e32 v18, 1, v18
	v_or_b32_sdwa v15, v15, v23 dst_sel:DWORD dst_unused:UNUSED_PAD src0_sel:DWORD src1_sel:WORD_1
	v_or_b32_sdwa v17, v17, v19 dst_sel:DWORD dst_unused:UNUSED_PAD src0_sel:DWORD src1_sel:WORD_1
	v_add3_u32 v18, 0, v18, v31
	ds_write_b64 v18, v[14:15]
	ds_write_b64 v18, v[16:17] offset:33024
	s_waitcnt vmcnt(2)
	v_and_b32_sdwa v16, v12, v237 dst_sel:DWORD dst_unused:UNUSED_PAD src0_sel:WORD_1 src1_sel:DWORD
	v_and_b32_sdwa v17, v10, v237 dst_sel:DWORD dst_unused:UNUSED_PAD src0_sel:WORD_1 src1_sel:DWORD
	v_add_u32_e32 v14, 0x2800, v30
	v_add3_u32 v19, v12, v16, s65
	v_add3_u32 v20, v10, v17, s65
	v_ashrrev_i32_e32 v18, 10, v14
	v_mov_b32_e32 v14, v10
	v_mov_b32_e32 v15, v12
	v_and_b32_e32 v17, 0xffff0000, v19
	v_and_b32_e32 v16, 0xffff0000, v20
	v_pk_add_f32 v[14:15], v[14:15], v[16:17] neg_lo:[0,1] neg_hi:[0,1]
	v_and_b32_sdwa v16, v11, v237 dst_sel:DWORD dst_unused:UNUSED_PAD src0_sel:WORD_1 src1_sel:DWORD
	v_and_b32_sdwa v10, v15, v237 dst_sel:DWORD dst_unused:UNUSED_PAD src0_sel:WORD_1 src1_sel:DWORD
	v_add3_u32 v15, v15, v10, s65
	v_and_b32_sdwa v10, v13, v237 dst_sel:DWORD dst_unused:UNUSED_PAD src0_sel:WORD_1 src1_sel:DWORD
	v_and_b32_sdwa v12, v14, v237 dst_sel:DWORD dst_unused:UNUSED_PAD src0_sel:WORD_1 src1_sel:DWORD
	v_add3_u32 v10, v13, v10, s65
	v_add3_u32 v16, v11, v16, s65
	v_add3_u32 v14, v14, v12, s65
	v_mov_b32_e32 v12, v11
	v_and_b32_e32 v11, 0xffff0000, v10
	v_and_b32_e32 v10, 0xffff0000, v16
	v_pk_add_f32 v[12:13], v[12:13], v[10:11] neg_lo:[0,1] neg_hi:[0,1]
	v_or_b32_sdwa v10, v10, v20 dst_sel:DWORD dst_unused:UNUSED_PAD src0_sel:DWORD src1_sel:WORD_1
	v_and_b32_sdwa v17, v12, v237 dst_sel:DWORD dst_unused:UNUSED_PAD src0_sel:WORD_1 src1_sel:DWORD
	v_add3_u32 v12, v12, v17, s65
	v_and_b32_sdwa v16, v13, v237 dst_sel:DWORD dst_unused:UNUSED_PAD src0_sel:WORD_1 src1_sel:DWORD
	v_and_b32_e32 v12, 0xffff0000, v12
	v_add3_u32 v13, v13, v16, s65
	v_or_b32_sdwa v12, v12, v14 dst_sel:DWORD dst_unused:UNUSED_PAD src0_sel:DWORD src1_sel:WORD_1
	v_mul_i32_i24_e32 v14, 0x408, v18
	v_and_b32_e32 v13, 0xffff0000, v13
	v_lshlrev_b32_e32 v14, 1, v14
	v_or_b32_sdwa v11, v11, v19 dst_sel:DWORD dst_unused:UNUSED_PAD src0_sel:DWORD src1_sel:WORD_1
	v_or_b32_sdwa v13, v13, v15 dst_sel:DWORD dst_unused:UNUSED_PAD src0_sel:DWORD src1_sel:WORD_1
	v_add3_u32 v14, 0, v14, v31
	ds_write_b64 v14, v[10:11]
	ds_write_b64 v14, v[12:13] offset:33024
	s_waitcnt vmcnt(1)
	v_and_b32_sdwa v12, v8, v237 dst_sel:DWORD dst_unused:UNUSED_PAD src0_sel:WORD_1 src1_sel:DWORD
	v_and_b32_sdwa v13, v6, v237 dst_sel:DWORD dst_unused:UNUSED_PAD src0_sel:WORD_1 src1_sel:DWORD
	v_add_u32_e32 v10, 0x3000, v30
	v_add3_u32 v15, v8, v12, s65
	v_add3_u32 v16, v6, v13, s65
	v_ashrrev_i32_e32 v14, 10, v10
	v_mov_b32_e32 v10, v6
	v_mov_b32_e32 v11, v8
	v_and_b32_e32 v13, 0xffff0000, v15
	v_and_b32_e32 v12, 0xffff0000, v16
	v_pk_add_f32 v[10:11], v[10:11], v[12:13] neg_lo:[0,1] neg_hi:[0,1]
	v_and_b32_sdwa v12, v7, v237 dst_sel:DWORD dst_unused:UNUSED_PAD src0_sel:WORD_1 src1_sel:DWORD
	v_and_b32_sdwa v6, v11, v237 dst_sel:DWORD dst_unused:UNUSED_PAD src0_sel:WORD_1 src1_sel:DWORD
	v_add3_u32 v11, v11, v6, s65
	v_and_b32_sdwa v6, v9, v237 dst_sel:DWORD dst_unused:UNUSED_PAD src0_sel:WORD_1 src1_sel:DWORD
	v_and_b32_sdwa v8, v10, v237 dst_sel:DWORD dst_unused:UNUSED_PAD src0_sel:WORD_1 src1_sel:DWORD
	v_add3_u32 v6, v9, v6, s65
	v_add3_u32 v12, v7, v12, s65
	v_add3_u32 v10, v10, v8, s65
	v_mov_b32_e32 v8, v7
	v_and_b32_e32 v7, 0xffff0000, v6
	v_and_b32_e32 v6, 0xffff0000, v12
	v_pk_add_f32 v[8:9], v[8:9], v[6:7] neg_lo:[0,1] neg_hi:[0,1]
	v_or_b32_sdwa v6, v6, v16 dst_sel:DWORD dst_unused:UNUSED_PAD src0_sel:DWORD src1_sel:WORD_1
	v_and_b32_sdwa v13, v8, v237 dst_sel:DWORD dst_unused:UNUSED_PAD src0_sel:WORD_1 src1_sel:DWORD
	v_add3_u32 v8, v8, v13, s65
	v_and_b32_sdwa v12, v9, v237 dst_sel:DWORD dst_unused:UNUSED_PAD src0_sel:WORD_1 src1_sel:DWORD
	v_and_b32_e32 v8, 0xffff0000, v8
	v_add3_u32 v9, v9, v12, s65
	v_or_b32_sdwa v8, v8, v10 dst_sel:DWORD dst_unused:UNUSED_PAD src0_sel:DWORD src1_sel:WORD_1
	v_mul_i32_i24_e32 v10, 0x408, v14
	v_and_b32_e32 v9, 0xffff0000, v9
	v_lshlrev_b32_e32 v10, 1, v10
	v_or_b32_sdwa v7, v7, v15 dst_sel:DWORD dst_unused:UNUSED_PAD src0_sel:DWORD src1_sel:WORD_1
	v_or_b32_sdwa v9, v9, v11 dst_sel:DWORD dst_unused:UNUSED_PAD src0_sel:DWORD src1_sel:WORD_1
	v_add3_u32 v10, 0, v10, v31
	ds_write_b64 v10, v[6:7]
	ds_write_b64 v10, v[8:9] offset:33024
	s_waitcnt vmcnt(0)
	v_and_b32_sdwa v8, v4, v237 dst_sel:DWORD dst_unused:UNUSED_PAD src0_sel:WORD_1 src1_sel:DWORD
	v_and_b32_sdwa v9, v2, v237 dst_sel:DWORD dst_unused:UNUSED_PAD src0_sel:WORD_1 src1_sel:DWORD
	v_add_u32_e32 v6, 0x3800, v30
	v_add3_u32 v11, v4, v8, s65
	v_add3_u32 v12, v2, v9, s65
	v_ashrrev_i32_e32 v10, 10, v6
	v_mov_b32_e32 v6, v2
	v_mov_b32_e32 v7, v4
	v_and_b32_e32 v9, 0xffff0000, v11
	v_and_b32_e32 v8, 0xffff0000, v12
	v_pk_add_f32 v[6:7], v[6:7], v[8:9] neg_lo:[0,1] neg_hi:[0,1]
	v_and_b32_sdwa v8, v3, v237 dst_sel:DWORD dst_unused:UNUSED_PAD src0_sel:WORD_1 src1_sel:DWORD
	v_and_b32_sdwa v2, v7, v237 dst_sel:DWORD dst_unused:UNUSED_PAD src0_sel:WORD_1 src1_sel:DWORD
	v_add3_u32 v7, v7, v2, s65
	v_and_b32_sdwa v2, v5, v237 dst_sel:DWORD dst_unused:UNUSED_PAD src0_sel:WORD_1 src1_sel:DWORD
	v_and_b32_sdwa v4, v6, v237 dst_sel:DWORD dst_unused:UNUSED_PAD src0_sel:WORD_1 src1_sel:DWORD
	v_add3_u32 v2, v5, v2, s65
	v_add3_u32 v8, v3, v8, s65
	v_add3_u32 v6, v6, v4, s65
	v_mov_b32_e32 v4, v3
	v_and_b32_e32 v3, 0xffff0000, v2
	v_and_b32_e32 v2, 0xffff0000, v8
	v_pk_add_f32 v[4:5], v[4:5], v[2:3] neg_lo:[0,1] neg_hi:[0,1]
	v_or_b32_sdwa v2, v2, v12 dst_sel:DWORD dst_unused:UNUSED_PAD src0_sel:DWORD src1_sel:WORD_1
	v_and_b32_sdwa v9, v4, v237 dst_sel:DWORD dst_unused:UNUSED_PAD src0_sel:WORD_1 src1_sel:DWORD
	v_add3_u32 v4, v4, v9, s65
	v_and_b32_e32 v4, 0xffff0000, v4
	v_and_b32_sdwa v8, v5, v237 dst_sel:DWORD dst_unused:UNUSED_PAD src0_sel:WORD_1 src1_sel:DWORD
	v_or_b32_sdwa v4, v4, v6 dst_sel:DWORD dst_unused:UNUSED_PAD src0_sel:DWORD src1_sel:WORD_1
	v_mul_i32_i24_e32 v6, 0x408, v10
	v_add3_u32 v5, v5, v8, s65
	v_lshlrev_b32_e32 v6, 1, v6
	v_and_b32_e32 v5, 0xffff0000, v5
	v_or_b32_sdwa v3, v3, v11 dst_sel:DWORD dst_unused:UNUSED_PAD src0_sel:DWORD src1_sel:WORD_1
	v_add3_u32 v6, 0, v6, v31
	v_or_b32_sdwa v5, v5, v7 dst_sel:DWORD dst_unused:UNUSED_PAD src0_sel:DWORD src1_sel:WORD_1
	ds_write_b64 v6, v[2:3]
	ds_write_b64 v6, v[4:5] offset:33024
	s_waitcnt lgkmcnt(0)
	s_barrier
	s_cbranch_scc1 .LBB0_733
	s_add_u32 s2, s0, 0x200000
	v_bfe_u32 v6, v32, 4, 2
	s_addc_u32 s3, s1, 0
	v_lshlrev_b32_e32 v2, 4, v6
	v_mov_b32_e32 v3, v195
	s_add_u32 s4, s0, 0x400000
	v_lshlrev_b32_e32 v194, 3, v6
	v_lshl_add_u64 v[4:5], s[0:1], 0, v[2:3]
	s_mov_b64 s[8:9], 0x4a000000
	s_addc_u32 s5, s1, 0
	v_lshl_add_u64 v[134:135], v[4:5], 0, s[8:9]
	v_lshl_add_u64 v[4:5], s[0:1], 0, v[194:195]
	s_mov_b64 s[0:1], 0x23000000
	v_lshl_add_u64 v[136:137], v[4:5], 0, s[0:1]
	s_lshl_b32 s0, s11, 7
	v_readlane_b32 s1, v254, 54
	v_and_b32_e32 v140, 15, v32
	s_add_i32 s8, s1, s0
	s_lshl_b32 s0, s11, 11
	v_readlane_b32 s1, v254, 55
	v_mul_u32_u24_e32 v3, 0x810, v140
	v_lshlrev_b32_e32 v142, 2, v6
	v_and_b32_e32 v143, 48, v32
	s_add_i32 s0, s1, s0
	s_lshl_b32 s7, s10, 3
	v_add3_u32 v141, 0, v3, v2
	v_or_b32_e32 v144, 4, v143
	v_or_b32_e32 v145, 8, v143
	v_or_b32_e32 v146, 12, v143
	s_lshl_b32 s9, s10, 7
	v_add_lshl_u32 v147, s8, v142, 4
	s_lshl_b32 s10, s10, 11
	v_lshl_add_u32 v148, v6, 6, s0
	s_mov_b32 s14, 0x3fb8aa3b
.LBB0_731:
	v_add_u32_e32 v2, s8, v140
	v_ashrrev_i32_e32 v3, 31, v2
	v_lshlrev_b64 v[138:139], 10, v[2:3]
	v_lshlrev_b64 v[2:3], 11, v[2:3]
	v_lshl_add_u64 v[2:3], v[134:135], 0, v[2:3]
	s_cmp_lg_u32 s101, 0
	s_cbranch_scc1 .Lrp2_skip
	global_load_dwordx4 v[130:133], v[2:3], off
	global_load_dwordx4 v[126:129], v[2:3], off offset:64
	global_load_dwordx4 v[122:125], v[2:3], off offset:128
	global_load_dwordx4 v[118:121], v[2:3], off offset:192
	global_load_dwordx4 v[114:117], v[2:3], off offset:256
	global_load_dwordx4 v[110:113], v[2:3], off offset:320
	global_load_dwordx4 v[106:109], v[2:3], off offset:384
	global_load_dwordx4 v[102:105], v[2:3], off offset:448
	global_load_dwordx4 v[98:101], v[2:3], off offset:512
	global_load_dwordx4 v[94:97], v[2:3], off offset:576
	global_load_dwordx4 v[90:93], v[2:3], off offset:640
	global_load_dwordx4 v[86:89], v[2:3], off offset:704
	global_load_dwordx4 v[82:85], v[2:3], off offset:768
	global_load_dwordx4 v[78:81], v[2:3], off offset:832
	global_load_dwordx4 v[74:77], v[2:3], off offset:896
	global_load_dwordx4 v[70:73], v[2:3], off offset:960
	global_load_dwordx4 v[66:69], v[2:3], off offset:1024
	global_load_dwordx4 v[62:65], v[2:3], off offset:1088
	global_load_dwordx4 v[58:61], v[2:3], off offset:1152
	global_load_dwordx4 v[54:57], v[2:3], off offset:1216
	global_load_dwordx4 v[50:53], v[2:3], off offset:1280
	global_load_dwordx4 v[46:49], v[2:3], off offset:1344
.Lrp2_skip:
	global_load_dwordx4 v[42:45], v[2:3], off offset:1408
	global_load_dwordx4 v[38:41], v[2:3], off offset:1472
	global_load_dwordx4 v[34:37], v[2:3], off offset:1536
	global_load_dwordx4 v[30:33], v[2:3], off offset:1600
	global_load_dwordx4 v[26:29], v[2:3], off offset:1664
	global_load_dwordx4 v[22:25], v[2:3], off offset:1728
	global_load_dwordx4 v[18:21], v[2:3], off offset:1792
	global_load_dwordx4 v[14:17], v[2:3], off offset:1856
	global_load_dwordx4 v[10:13], v[2:3], off offset:1920
	global_load_dwordx4 v[6:9], v[2:3], off offset:1984
	s_mov_b32 s101, 0
	ds_read_b128 v[2:5], v141
	ds_read_b128 v[150:153], v141 offset:33024
	v_lshl_add_u64 v[138:139], v[136:137], 0, v[138:139]
	s_waitcnt vmcnt(31) lgkmcnt(1)
	v_mfma_f32_16x16x32_bf16 v[2:5], v[130:133], v[2:5], 0
	v_lshlrev_b32_e32 v149, 16, v130
	v_and_b32_e32 v154, 0xffff0000, v132
	v_and_b32_e32 v156, 0xffff0000, v133
	s_waitcnt lgkmcnt(0)
	v_mfma_f32_16x16x32_bf16 v[2:5], v[130:133], v[150:153], v[2:5]
	v_and_b32_e32 v150, 0xffff0000, v130
	v_and_b32_e32 v152, 0xffff0000, v131
	v_mul_f32_e32 v150, v150, v150
	v_lshlrev_b32_e32 v151, 16, v131
	v_fmac_f32_e32 v150, v149, v149
	v_mul_f32_e32 v149, v152, v152
	v_fmac_f32_e32 v149, v151, v151
	v_lshlrev_b32_e32 v153, 16, v132
	v_lshlrev_b32_e32 v155, 16, v133
	v_add_f32_e32 v149, v150, v149
	v_mul_f32_e32 v150, v154, v154
	v_mul_f32_e32 v151, v156, v156
	v_fmac_f32_e32 v150, v153, v153
	v_fmac_f32_e32 v151, v155, v155
	v_add_f32_e32 v150, v150, v151
	v_add_f32_e32 v149, v149, v150
	ds_read_b128 v[150:153], v141 offset:33088
	ds_read_b128 v[154:157], v141 offset:64
	s_waitcnt vmcnt(30) lgkmcnt(0)
	v_mfma_f32_16x16x32_bf16 v[2:5], v[126:129], v[154:157], v[2:5]
	v_and_b32_e32 v155, 0xffff0000, v128
	v_and_b32_e32 v157, 0xffff0000, v129
	v_lshlrev_b32_e32 v154, 16, v128
	v_mfma_f32_16x16x32_bf16 v[2:5], v[126:129], v[150:153], v[2:5]
	v_and_b32_e32 v151, 0xffff0000, v126
	v_lshlrev_b32_e32 v150, 16, v126
	v_and_b32_e32 v153, 0xffff0000, v127
	v_mul_f32_e32 v151, v151, v151
	v_lshlrev_b32_e32 v152, 16, v127
	v_fmac_f32_e32 v151, v150, v150
	v_mul_f32_e32 v150, v153, v153
	v_fmac_f32_e32 v150, v152, v152
	v_lshlrev_b32_e32 v156, 16, v129
	v_add_f32_e32 v150, v151, v150
	v_mul_f32_e32 v151, v155, v155
	v_mul_f32_e32 v152, v157, v157
	v_fmac_f32_e32 v151, v154, v154
	v_fmac_f32_e32 v152, v156, v156
	v_add_f32_e32 v151, v151, v152
	v_add_f32_e32 v150, v150, v151
	v_add_f32_e32 v149, v149, v150
	ds_read_b128 v[150:153], v141 offset:33152
	ds_read_b128 v[154:157], v141 offset:128
	s_waitcnt vmcnt(29) lgkmcnt(0)
	v_mfma_f32_16x16x32_bf16 v[2:5], v[122:125], v[154:157], v[2:5]
	v_and_b32_e32 v155, 0xffff0000, v124
	v_and_b32_e32 v157, 0xffff0000, v125
	v_lshlrev_b32_e32 v154, 16, v124
	v_mfma_f32_16x16x32_bf16 v[2:5], v[122:125], v[150:153], v[2:5]
	v_and_b32_e32 v151, 0xffff0000, v122
	v_lshlrev_b32_e32 v150, 16, v122
	v_and_b32_e32 v153, 0xffff0000, v123
	v_mul_f32_e32 v151, v151, v151
	v_lshlrev_b32_e32 v152, 16, v123
	v_fmac_f32_e32 v151, v150, v150
	v_mul_f32_e32 v150, v153, v153
	v_fmac_f32_e32 v150, v152, v152
	v_lshlrev_b32_e32 v156, 16, v125
	v_add_f32_e32 v150, v151, v150
	v_mul_f32_e32 v151, v155, v155
	v_mul_f32_e32 v152, v157, v157
	v_fmac_f32_e32 v151, v154, v154
	v_fmac_f32_e32 v152, v156, v156
	v_add_f32_e32 v151, v151, v152
	v_add_f32_e32 v150, v150, v151
	v_add_f32_e32 v149, v149, v150
	ds_read_b128 v[150:153], v141 offset:33216
	ds_read_b128 v[154:157], v141 offset:192
	s_waitcnt vmcnt(28) lgkmcnt(0)
	v_mfma_f32_16x16x32_bf16 v[2:5], v[118:121], v[154:157], v[2:5]
	v_mfma_f32_16x16x32_bf16 v[2:5], v[118:121], v[150:153], v[2:5]
	v_and_b32_e32 v151, 0xffff0000, v118
	v_lshlrev_b32_e32 v150, 16, v118
	v_mul_f32_e32 v151, v151, v151
	v_and_b32_e32 v152, 0xffff0000, v119
	v_fmac_f32_e32 v151, v150, v150
	v_lshlrev_b32_e32 v150, 16, v119
	v_mul_f32_e32 v152, v152, v152
	v_fmac_f32_e32 v152, v150, v150
	v_add_f32_e32 v150, v151, v152
	v_and_b32_e32 v152, 0xffff0000, v120
	v_lshlrev_b32_e32 v151, 16, v120
	v_mul_f32_e32 v152, v152, v152
	v_and_b32_e32 v153, 0xffff0000, v121
	v_fmac_f32_e32 v152, v151, v151
	v_lshlrev_b32_e32 v151, 16, v121
	v_mul_f32_e32 v153, v153, v153
	v_fmac_f32_e32 v153, v151, v151
	v_add_f32_e32 v151, v152, v153
	v_add_f32_e32 v150, v150, v151
	v_add_f32_e32 v149, v149, v150
	ds_read_b128 v[150:153], v141 offset:256
	ds_read_b128 v[154:157], v141 offset:33280
	s_waitcnt vmcnt(27) lgkmcnt(1)
	v_mfma_f32_16x16x32_bf16 v[2:5], v[114:117], v[150:153], v[2:5]
	v_and_b32_e32 v151, 0xffff0000, v114
	v_lshlrev_b32_e32 v150, 16, v114
	v_and_b32_e32 v153, 0xffff0000, v115
	v_mul_f32_e32 v151, v151, v151
	v_lshlrev_b32_e32 v152, 16, v115
	v_fmac_f32_e32 v151, v150, v150
	v_mul_f32_e32 v150, v153, v153
	s_waitcnt lgkmcnt(0)
	v_mfma_f32_16x16x32_bf16 v[2:5], v[114:117], v[154:157], v[2:5]
	v_and_b32_e32 v155, 0xffff0000, v116
	v_and_b32_e32 v157, 0xffff0000, v117
	v_fmac_f32_e32 v150, v152, v152
	v_lshlrev_b32_e32 v154, 16, v116
	v_lshlrev_b32_e32 v156, 16, v117
	v_add_f32_e32 v150, v151, v150
	v_mul_f32_e32 v151, v155, v155
	v_mul_f32_e32 v152, v157, v157
	v_fmac_f32_e32 v151, v154, v154
	v_fmac_f32_e32 v152, v156, v156
	v_add_f32_e32 v151, v151, v152
	v_add_f32_e32 v150, v150, v151
	v_add_f32_e32 v149, v150, v149
	ds_read_b128 v[150:153], v141 offset:33344
	ds_read_b128 v[154:157], v141 offset:320
	s_waitcnt vmcnt(26) lgkmcnt(0)
	v_mfma_f32_16x16x32_bf16 v[2:5], v[110:113], v[154:157], v[2:5]
	v_and_b32_e32 v155, 0xffff0000, v112
	v_and_b32_e32 v157, 0xffff0000, v113
	v_lshlrev_b32_e32 v154, 16, v112
	v_mfma_f32_16x16x32_bf16 v[2:5], v[110:113], v[150:153], v[2:5]
	v_and_b32_e32 v151, 0xffff0000, v110
	v_lshlrev_b32_e32 v150, 16, v110
	v_and_b32_e32 v153, 0xffff0000, v111
	v_mul_f32_e32 v151, v151, v151
	v_lshlrev_b32_e32 v152, 16, v111
	v_fmac_f32_e32 v151, v150, v150
	v_mul_f32_e32 v150, v153, v153
	v_fmac_f32_e32 v150, v152, v152
	v_lshlrev_b32_e32 v156, 16, v113
	v_add_f32_e32 v150, v151, v150
	v_mul_f32_e32 v151, v155, v155
	v_mul_f32_e32 v152, v157, v157
	v_fmac_f32_e32 v151, v154, v154
	v_fmac_f32_e32 v152, v156, v156
	v_add_f32_e32 v151, v151, v152
	v_add_f32_e32 v150, v150, v151
	v_add_f32_e32 v149, v150, v149
	ds_read_b128 v[150:153], v141 offset:33408
	ds_read_b128 v[154:157], v141 offset:384
	s_waitcnt vmcnt(25) lgkmcnt(0)
	v_mfma_f32_16x16x32_bf16 v[2:5], v[106:109], v[154:157], v[2:5]
	v_and_b32_e32 v155, 0xffff0000, v108
	v_and_b32_e32 v157, 0xffff0000, v109
	v_lshlrev_b32_e32 v154, 16, v108
	v_mfma_f32_16x16x32_bf16 v[2:5], v[106:109], v[150:153], v[2:5]
	v_and_b32_e32 v151, 0xffff0000, v106
	v_lshlrev_b32_e32 v150, 16, v106
	v_and_b32_e32 v153, 0xffff0000, v107
	v_mul_f32_e32 v151, v151, v151
	v_lshlrev_b32_e32 v152, 16, v107
	v_fmac_f32_e32 v151, v150, v150
	v_mul_f32_e32 v150, v153, v153
	v_fmac_f32_e32 v150, v152, v152
	v_lshlrev_b32_e32 v156, 16, v109
	v_add_f32_e32 v150, v151, v150
	v_mul_f32_e32 v151, v155, v155
	v_mul_f32_e32 v152, v157, v157
	v_fmac_f32_e32 v151, v154, v154
	v_fmac_f32_e32 v152, v156, v156
	v_add_f32_e32 v151, v151, v152
	v_add_f32_e32 v150, v150, v151
	v_add_f32_e32 v149, v150, v149
	ds_read_b128 v[150:153], v141 offset:33472
	ds_read_b128 v[154:157], v141 offset:448
	s_waitcnt vmcnt(24) lgkmcnt(0)
	v_mfma_f32_16x16x32_bf16 v[2:5], v[102:105], v[154:157], v[2:5]
	v_mfma_f32_16x16x32_bf16 v[2:5], v[102:105], v[150:153], v[2:5]
	v_and_b32_e32 v151, 0xffff0000, v102
	v_lshlrev_b32_e32 v150, 16, v102
	v_mul_f32_e32 v151, v151, v151
	v_and_b32_e32 v152, 0xffff0000, v103
	v_fmac_f32_e32 v151, v150, v150
	v_lshlrev_b32_e32 v150, 16, v103
	v_mul_f32_e32 v152, v152, v152
	v_fmac_f32_e32 v152, v150, v150
	v_add_f32_e32 v150, v151, v152
	v_and_b32_e32 v152, 0xffff0000, v104
	v_lshlrev_b32_e32 v151, 16, v104
	v_mul_f32_e32 v152, v152, v152
	v_and_b32_e32 v153, 0xffff0000, v105
	v_fmac_f32_e32 v152, v151, v151
	v_lshlrev_b32_e32 v151, 16, v105
	v_mul_f32_e32 v153, v153, v153
	v_fmac_f32_e32 v153, v151, v151
	v_add_f32_e32 v151, v152, v153
	v_add_f32_e32 v150, v150, v151
	v_add_f32_e32 v149, v150, v149
	ds_read_b128 v[150:153], v141 offset:512
	ds_read_b128 v[154:157], v141 offset:33536
	s_waitcnt vmcnt(23) lgkmcnt(1)
	v_mfma_f32_16x16x32_bf16 v[2:5], v[98:101], v[150:153], v[2:5]
	v_and_b32_e32 v151, 0xffff0000, v98
	v_lshlrev_b32_e32 v150, 16, v98
	v_and_b32_e32 v153, 0xffff0000, v99
	v_mul_f32_e32 v151, v151, v151
	v_lshlrev_b32_e32 v152, 16, v99
	v_fmac_f32_e32 v151, v150, v150
	v_mul_f32_e32 v150, v153, v153
	s_waitcnt lgkmcnt(0)
	v_mfma_f32_16x16x32_bf16 v[2:5], v[98:101], v[154:157], v[2:5]
	v_and_b32_e32 v155, 0xffff0000, v100
	v_and_b32_e32 v157, 0xffff0000, v101
	v_fmac_f32_e32 v150, v152, v152
	v_lshlrev_b32_e32 v154, 16, v100
	v_lshlrev_b32_e32 v156, 16, v101
	v_add_f32_e32 v150, v151, v150
	v_mul_f32_e32 v151, v155, v155
	v_mul_f32_e32 v152, v157, v157
	v_fmac_f32_e32 v151, v154, v154
	v_fmac_f32_e32 v152, v156, v156
	v_add_f32_e32 v151, v151, v152
	v_add_f32_e32 v150, v150, v151
	v_add_f32_e32 v149, v150, v149
	ds_read_b128 v[150:153], v141 offset:33600
	ds_read_b128 v[154:157], v141 offset:576
	s_waitcnt vmcnt(22) lgkmcnt(0)
	v_mfma_f32_16x16x32_bf16 v[2:5], v[94:97], v[154:157], v[2:5]
	v_and_b32_e32 v155, 0xffff0000, v96
	v_and_b32_e32 v157, 0xffff0000, v97
	v_lshlrev_b32_e32 v154, 16, v96
	v_mfma_f32_16x16x32_bf16 v[2:5], v[94:97], v[150:153], v[2:5]
	v_and_b32_e32 v151, 0xffff0000, v94
	v_lshlrev_b32_e32 v150, 16, v94
	v_and_b32_e32 v153, 0xffff0000, v95
	v_mul_f32_e32 v151, v151, v151
	v_lshlrev_b32_e32 v152, 16, v95
	v_fmac_f32_e32 v151, v150, v150
	v_mul_f32_e32 v150, v153, v153
	v_fmac_f32_e32 v150, v152, v152
	v_lshlrev_b32_e32 v156, 16, v97
	v_add_f32_e32 v150, v151, v150
	v_mul_f32_e32 v151, v155, v155
	v_mul_f32_e32 v152, v157, v157
	v_fmac_f32_e32 v151, v154, v154
	v_fmac_f32_e32 v152, v156, v156
	v_add_f32_e32 v151, v151, v152
	v_add_f32_e32 v150, v150, v151
	v_add_f32_e32 v149, v150, v149
	ds_read_b128 v[150:153], v141 offset:33664
	ds_read_b128 v[154:157], v141 offset:640
	s_waitcnt vmcnt(21) lgkmcnt(0)
	v_mfma_f32_16x16x32_bf16 v[2:5], v[90:93], v[154:157], v[2:5]
	v_and_b32_e32 v155, 0xffff0000, v92
	v_and_b32_e32 v157, 0xffff0000, v93
	v_lshlrev_b32_e32 v154, 16, v92
	v_mfma_f32_16x16x32_bf16 v[2:5], v[90:93], v[150:153], v[2:5]
	v_and_b32_e32 v151, 0xffff0000, v90
	v_lshlrev_b32_e32 v150, 16, v90
	v_and_b32_e32 v153, 0xffff0000, v91
	v_mul_f32_e32 v151, v151, v151
	v_lshlrev_b32_e32 v152, 16, v91
	v_fmac_f32_e32 v151, v150, v150
	v_mul_f32_e32 v150, v153, v153
	v_fmac_f32_e32 v150, v152, v152
	v_lshlrev_b32_e32 v156, 16, v93
	v_add_f32_e32 v150, v151, v150
	v_mul_f32_e32 v151, v155, v155
	v_mul_f32_e32 v152, v157, v157
	v_fmac_f32_e32 v151, v154, v154
	v_fmac_f32_e32 v152, v156, v156
	v_add_f32_e32 v151, v151, v152
	v_add_f32_e32 v150, v150, v151
	v_add_f32_e32 v149, v150, v149
	ds_read_b128 v[150:153], v141 offset:33728
	ds_read_b128 v[154:157], v141 offset:704
	s_waitcnt vmcnt(20) lgkmcnt(0)
	v_mfma_f32_16x16x32_bf16 v[2:5], v[86:89], v[154:157], v[2:5]
	v_mfma_f32_16x16x32_bf16 v[2:5], v[86:89], v[150:153], v[2:5]
	v_and_b32_e32 v151, 0xffff0000, v86
	v_lshlrev_b32_e32 v150, 16, v86
	v_mul_f32_e32 v151, v151, v151
	v_and_b32_e32 v152, 0xffff0000, v87
	v_fmac_f32_e32 v151, v150, v150
	v_lshlrev_b32_e32 v150, 16, v87
	v_mul_f32_e32 v152, v152, v152
	v_fmac_f32_e32 v152, v150, v150
	v_add_f32_e32 v150, v151, v152
	v_and_b32_e32 v152, 0xffff0000, v88
	v_lshlrev_b32_e32 v151, 16, v88
	v_mul_f32_e32 v152, v152, v152
	v_and_b32_e32 v153, 0xffff0000, v89
	v_fmac_f32_e32 v152, v151, v151
	v_lshlrev_b32_e32 v151, 16, v89
	v_mul_f32_e32 v153, v153, v153
	v_fmac_f32_e32 v153, v151, v151
	v_add_f32_e32 v151, v152, v153
	v_add_f32_e32 v150, v150, v151
	v_add_f32_e32 v149, v150, v149
	ds_read_b128 v[150:153], v141 offset:768
	ds_read_b128 v[154:157], v141 offset:33792
	s_waitcnt vmcnt(19) lgkmcnt(1)
	v_mfma_f32_16x16x32_bf16 v[2:5], v[82:85], v[150:153], v[2:5]
	v_and_b32_e32 v151, 0xffff0000, v82
	v_lshlrev_b32_e32 v150, 16, v82
	v_and_b32_e32 v153, 0xffff0000, v83
	v_mul_f32_e32 v151, v151, v151
	v_lshlrev_b32_e32 v152, 16, v83
	v_fmac_f32_e32 v151, v150, v150
	v_mul_f32_e32 v150, v153, v153
	s_waitcnt lgkmcnt(0)
	v_mfma_f32_16x16x32_bf16 v[2:5], v[82:85], v[154:157], v[2:5]
	v_and_b32_e32 v155, 0xffff0000, v84
	v_and_b32_e32 v157, 0xffff0000, v85
	v_fmac_f32_e32 v150, v152, v152
	v_lshlrev_b32_e32 v154, 16, v84
	v_lshlrev_b32_e32 v156, 16, v85
	v_add_f32_e32 v150, v151, v150
	v_mul_f32_e32 v151, v155, v155
	v_mul_f32_e32 v152, v157, v157
	v_fmac_f32_e32 v151, v154, v154
	v_fmac_f32_e32 v152, v156, v156
	v_add_f32_e32 v151, v151, v152
	v_add_f32_e32 v150, v150, v151
	v_add_f32_e32 v149, v150, v149
	ds_read_b128 v[150:153], v141 offset:33856
	ds_read_b128 v[154:157], v141 offset:832
	s_waitcnt vmcnt(18) lgkmcnt(0)
	v_mfma_f32_16x16x32_bf16 v[2:5], v[78:81], v[154:157], v[2:5]
	v_and_b32_e32 v155, 0xffff0000, v80
	v_and_b32_e32 v157, 0xffff0000, v81
	v_lshlrev_b32_e32 v154, 16, v80
	v_mfma_f32_16x16x32_bf16 v[2:5], v[78:81], v[150:153], v[2:5]
	v_and_b32_e32 v151, 0xffff0000, v78
	v_lshlrev_b32_e32 v150, 16, v78
	v_and_b32_e32 v153, 0xffff0000, v79
	v_mul_f32_e32 v151, v151, v151
	v_lshlrev_b32_e32 v152, 16, v79
	v_fmac_f32_e32 v151, v150, v150
	v_mul_f32_e32 v150, v153, v153
	v_fmac_f32_e32 v150, v152, v152
	v_lshlrev_b32_e32 v156, 16, v81
	v_add_f32_e32 v150, v151, v150
	v_mul_f32_e32 v151, v155, v155
	v_mul_f32_e32 v152, v157, v157
	v_fmac_f32_e32 v151, v154, v154
	v_fmac_f32_e32 v152, v156, v156
	v_add_f32_e32 v151, v151, v152
	v_add_f32_e32 v150, v150, v151
	v_add_f32_e32 v149, v150, v149
	ds_read_b128 v[150:153], v141 offset:33920
	ds_read_b128 v[154:157], v141 offset:896
	s_waitcnt vmcnt(17) lgkmcnt(0)
	v_mfma_f32_16x16x32_bf16 v[2:5], v[74:77], v[154:157], v[2:5]
	v_and_b32_e32 v155, 0xffff0000, v76
	v_and_b32_e32 v157, 0xffff0000, v77
	v_lshlrev_b32_e32 v154, 16, v76
	v_mfma_f32_16x16x32_bf16 v[2:5], v[74:77], v[150:153], v[2:5]
	v_and_b32_e32 v151, 0xffff0000, v74
	v_lshlrev_b32_e32 v150, 16, v74
	v_and_b32_e32 v153, 0xffff0000, v75
	v_mul_f32_e32 v151, v151, v151
	v_lshlrev_b32_e32 v152, 16, v75
	v_fmac_f32_e32 v151, v150, v150
	v_mul_f32_e32 v150, v153, v153
	v_fmac_f32_e32 v150, v152, v152
	v_lshlrev_b32_e32 v156, 16, v77
	v_add_f32_e32 v150, v151, v150
	v_mul_f32_e32 v151, v155, v155
	v_mul_f32_e32 v152, v157, v157
	v_fmac_f32_e32 v151, v154, v154
	v_fmac_f32_e32 v152, v156, v156
	v_add_f32_e32 v151, v151, v152
	v_add_f32_e32 v150, v150, v151
	v_add_f32_e32 v149, v150, v149
	ds_read_b128 v[150:153], v141 offset:33984
	ds_read_b128 v[154:157], v141 offset:960
	s_waitcnt vmcnt(16) lgkmcnt(0)
	v_mfma_f32_16x16x32_bf16 v[2:5], v[70:73], v[154:157], v[2:5]
	v_mfma_f32_16x16x32_bf16 v[2:5], v[70:73], v[150:153], v[2:5]
	v_and_b32_e32 v151, 0xffff0000, v70
	v_lshlrev_b32_e32 v150, 16, v70
	v_mul_f32_e32 v151, v151, v151
	v_and_b32_e32 v152, 0xffff0000, v71
	v_fmac_f32_e32 v151, v150, v150
	v_lshlrev_b32_e32 v150, 16, v71
	v_mul_f32_e32 v152, v152, v152
	v_fmac_f32_e32 v152, v150, v150
	v_add_f32_e32 v150, v151, v152
	v_and_b32_e32 v152, 0xffff0000, v72
	v_lshlrev_b32_e32 v151, 16, v72
	v_mul_f32_e32 v152, v152, v152
	v_and_b32_e32 v153, 0xffff0000, v73
	v_fmac_f32_e32 v152, v151, v151
	v_lshlrev_b32_e32 v151, 16, v73
	v_mul_f32_e32 v153, v153, v153
	v_fmac_f32_e32 v153, v151, v151
	v_add_f32_e32 v151, v152, v153
	v_add_f32_e32 v150, v150, v151
	v_add_f32_e32 v149, v150, v149
	ds_read_b128 v[150:153], v141 offset:1024
	ds_read_b128 v[154:157], v141 offset:34048
	s_waitcnt vmcnt(15) lgkmcnt(1)
	v_mfma_f32_16x16x32_bf16 v[2:5], v[66:69], v[150:153], v[2:5]
	v_and_b32_e32 v151, 0xffff0000, v66
	v_lshlrev_b32_e32 v150, 16, v66
	v_and_b32_e32 v153, 0xffff0000, v67
	v_mul_f32_e32 v151, v151, v151
	v_lshlrev_b32_e32 v152, 16, v67
	v_fmac_f32_e32 v151, v150, v150
	v_mul_f32_e32 v150, v153, v153
	s_waitcnt lgkmcnt(0)
	v_mfma_f32_16x16x32_bf16 v[2:5], v[66:69], v[154:157], v[2:5]
	v_and_b32_e32 v155, 0xffff0000, v68
	v_and_b32_e32 v157, 0xffff0000, v69
	v_fmac_f32_e32 v150, v152, v152
	v_lshlrev_b32_e32 v154, 16, v68
	v_lshlrev_b32_e32 v156, 16, v69
	v_add_f32_e32 v150, v151, v150
	v_mul_f32_e32 v151, v155, v155
	v_mul_f32_e32 v152, v157, v157
	v_fmac_f32_e32 v151, v154, v154
	v_fmac_f32_e32 v152, v156, v156
	v_add_f32_e32 v151, v151, v152
	v_add_f32_e32 v150, v150, v151
	v_add_f32_e32 v149, v150, v149
	ds_read_b128 v[150:153], v141 offset:34112
	ds_read_b128 v[154:157], v141 offset:1088
	s_waitcnt vmcnt(14) lgkmcnt(0)
	v_mfma_f32_16x16x32_bf16 v[2:5], v[62:65], v[154:157], v[2:5]
	v_and_b32_e32 v155, 0xffff0000, v64
	v_and_b32_e32 v157, 0xffff0000, v65
	v_lshlrev_b32_e32 v154, 16, v64
	v_mfma_f32_16x16x32_bf16 v[2:5], v[62:65], v[150:153], v[2:5]
	v_and_b32_e32 v151, 0xffff0000, v62
	v_lshlrev_b32_e32 v150, 16, v62
	v_and_b32_e32 v153, 0xffff0000, v63
	v_mul_f32_e32 v151, v151, v151
	v_lshlrev_b32_e32 v152, 16, v63
	v_fmac_f32_e32 v151, v150, v150
	v_mul_f32_e32 v150, v153, v153
	v_fmac_f32_e32 v150, v152, v152
	v_lshlrev_b32_e32 v156, 16, v65
	v_add_f32_e32 v150, v151, v150
	v_mul_f32_e32 v151, v155, v155
	v_mul_f32_e32 v152, v157, v157
	v_fmac_f32_e32 v151, v154, v154
	v_fmac_f32_e32 v152, v156, v156
	v_add_f32_e32 v151, v151, v152
	v_add_f32_e32 v150, v150, v151
	v_add_f32_e32 v149, v150, v149
	ds_read_b128 v[150:153], v141 offset:34176
	ds_read_b128 v[154:157], v141 offset:1152
	s_waitcnt vmcnt(13) lgkmcnt(0)
	v_mfma_f32_16x16x32_bf16 v[2:5], v[58:61], v[154:157], v[2:5]
	v_and_b32_e32 v155, 0xffff0000, v60
	v_and_b32_e32 v157, 0xffff0000, v61
	v_lshlrev_b32_e32 v154, 16, v60
	v_mfma_f32_16x16x32_bf16 v[2:5], v[58:61], v[150:153], v[2:5]
	v_and_b32_e32 v151, 0xffff0000, v58
	v_lshlrev_b32_e32 v150, 16, v58
	v_and_b32_e32 v153, 0xffff0000, v59
	v_mul_f32_e32 v151, v151, v151
	v_lshlrev_b32_e32 v152, 16, v59
	v_fmac_f32_e32 v151, v150, v150
	v_mul_f32_e32 v150, v153, v153
	v_fmac_f32_e32 v150, v152, v152
	v_lshlrev_b32_e32 v156, 16, v61
	v_add_f32_e32 v150, v151, v150
	v_mul_f32_e32 v151, v155, v155
	v_mul_f32_e32 v152, v157, v157
	v_fmac_f32_e32 v151, v154, v154
	v_fmac_f32_e32 v152, v156, v156
	v_add_f32_e32 v151, v151, v152
	v_add_f32_e32 v150, v150, v151
	v_add_f32_e32 v149, v150, v149
	ds_read_b128 v[150:153], v141 offset:34240
	ds_read_b128 v[154:157], v141 offset:1216
	s_waitcnt vmcnt(12) lgkmcnt(0)
	v_mfma_f32_16x16x32_bf16 v[2:5], v[54:57], v[154:157], v[2:5]
	v_mfma_f32_16x16x32_bf16 v[2:5], v[54:57], v[150:153], v[2:5]
	v_and_b32_e32 v151, 0xffff0000, v54
	v_lshlrev_b32_e32 v150, 16, v54
	v_mul_f32_e32 v151, v151, v151
	v_and_b32_e32 v152, 0xffff0000, v55
	v_fmac_f32_e32 v151, v150, v150
	v_lshlrev_b32_e32 v150, 16, v55
	v_mul_f32_e32 v152, v152, v152
	v_fmac_f32_e32 v152, v150, v150
	v_add_f32_e32 v150, v151, v152
	v_and_b32_e32 v152, 0xffff0000, v56
	v_lshlrev_b32_e32 v151, 16, v56
	v_mul_f32_e32 v152, v152, v152
	v_and_b32_e32 v153, 0xffff0000, v57
	v_fmac_f32_e32 v152, v151, v151
	v_lshlrev_b32_e32 v151, 16, v57
	v_mul_f32_e32 v153, v153, v153
	v_fmac_f32_e32 v153, v151, v151
	v_add_f32_e32 v151, v152, v153
	v_add_f32_e32 v150, v150, v151
	v_add_f32_e32 v149, v150, v149
	ds_read_b128 v[150:153], v141 offset:1280
	ds_read_b128 v[154:157], v141 offset:34304
	s_waitcnt vmcnt(11) lgkmcnt(1)
	v_mfma_f32_16x16x32_bf16 v[2:5], v[50:53], v[150:153], v[2:5]
	v_and_b32_e32 v151, 0xffff0000, v50
	v_lshlrev_b32_e32 v150, 16, v50
	v_and_b32_e32 v153, 0xffff0000, v51
	v_mul_f32_e32 v151, v151, v151
	v_lshlrev_b32_e32 v152, 16, v51
	v_fmac_f32_e32 v151, v150, v150
	v_mul_f32_e32 v150, v153, v153
	s_waitcnt lgkmcnt(0)
	v_mfma_f32_16x16x32_bf16 v[2:5], v[50:53], v[154:157], v[2:5]
	v_and_b32_e32 v155, 0xffff0000, v52
	v_and_b32_e32 v157, 0xffff0000, v53
	v_fmac_f32_e32 v150, v152, v152
	v_lshlrev_b32_e32 v154, 16, v52
	v_lshlrev_b32_e32 v156, 16, v53
	v_add_f32_e32 v150, v151, v150
	v_mul_f32_e32 v151, v155, v155
	v_mul_f32_e32 v152, v157, v157
	v_fmac_f32_e32 v151, v154, v154
	v_fmac_f32_e32 v152, v156, v156
	v_add_f32_e32 v151, v151, v152
	v_add_f32_e32 v150, v150, v151
	v_add_f32_e32 v149, v150, v149
	ds_read_b128 v[150:153], v141 offset:34368
	ds_read_b128 v[154:157], v141 offset:1344
	s_waitcnt vmcnt(10) lgkmcnt(0)
	v_mfma_f32_16x16x32_bf16 v[2:5], v[46:49], v[154:157], v[2:5]
	v_and_b32_e32 v155, 0xffff0000, v48
	v_and_b32_e32 v157, 0xffff0000, v49
	v_lshlrev_b32_e32 v154, 16, v48
	v_mfma_f32_16x16x32_bf16 v[2:5], v[46:49], v[150:153], v[2:5]
	v_and_b32_e32 v151, 0xffff0000, v46
	v_lshlrev_b32_e32 v150, 16, v46
	v_and_b32_e32 v153, 0xffff0000, v47
	v_mul_f32_e32 v151, v151, v151
	v_lshlrev_b32_e32 v152, 16, v47
	v_fmac_f32_e32 v151, v150, v150
	v_mul_f32_e32 v150, v153, v153
	v_fmac_f32_e32 v150, v152, v152
	v_lshlrev_b32_e32 v156, 16, v49
	v_add_f32_e32 v150, v151, v150
	v_mul_f32_e32 v151, v155, v155
	v_mul_f32_e32 v152, v157, v157
	v_fmac_f32_e32 v151, v154, v154
	v_fmac_f32_e32 v152, v156, v156
	v_add_f32_e32 v151, v151, v152
	v_add_f32_e32 v150, v150, v151
	v_add_f32_e32 v149, v150, v149
	ds_read_b128 v[150:153], v141 offset:34432
	ds_read_b128 v[154:157], v141 offset:1408
	s_waitcnt vmcnt(9) lgkmcnt(0)
	v_mfma_f32_16x16x32_bf16 v[2:5], v[42:45], v[154:157], v[2:5]
	v_and_b32_e32 v155, 0xffff0000, v44
	v_and_b32_e32 v157, 0xffff0000, v45
	v_lshlrev_b32_e32 v154, 16, v44
	v_mfma_f32_16x16x32_bf16 v[2:5], v[42:45], v[150:153], v[2:5]
	v_and_b32_e32 v151, 0xffff0000, v42
	v_lshlrev_b32_e32 v150, 16, v42
	v_and_b32_e32 v153, 0xffff0000, v43
	v_mul_f32_e32 v151, v151, v151
	v_lshlrev_b32_e32 v152, 16, v43
	v_fmac_f32_e32 v151, v150, v150
	v_mul_f32_e32 v150, v153, v153
	v_fmac_f32_e32 v150, v152, v152
	v_lshlrev_b32_e32 v156, 16, v45
	v_add_f32_e32 v150, v151, v150
	v_mul_f32_e32 v151, v155, v155
	v_mul_f32_e32 v152, v157, v157
	v_fmac_f32_e32 v151, v154, v154
	v_fmac_f32_e32 v152, v156, v156
	v_add_f32_e32 v151, v151, v152
	v_add_f32_e32 v150, v150, v151
	v_add_f32_e32 v149, v150, v149
	ds_read_b128 v[150:153], v141 offset:34496
	ds_read_b128 v[154:157], v141 offset:1472
	s_waitcnt vmcnt(8) lgkmcnt(0)
	v_mfma_f32_16x16x32_bf16 v[2:5], v[38:41], v[154:157], v[2:5]
	v_mfma_f32_16x16x32_bf16 v[2:5], v[38:41], v[150:153], v[2:5]
	v_and_b32_e32 v151, 0xffff0000, v38
	v_lshlrev_b32_e32 v150, 16, v38
	v_mul_f32_e32 v151, v151, v151
	v_and_b32_e32 v152, 0xffff0000, v39
	v_fmac_f32_e32 v151, v150, v150
	v_lshlrev_b32_e32 v150, 16, v39
	v_mul_f32_e32 v152, v152, v152
	v_fmac_f32_e32 v152, v150, v150
	v_add_f32_e32 v150, v151, v152
	v_and_b32_e32 v152, 0xffff0000, v40
	v_lshlrev_b32_e32 v151, 16, v40
	v_mul_f32_e32 v152, v152, v152
	v_and_b32_e32 v153, 0xffff0000, v41
	v_fmac_f32_e32 v152, v151, v151
	v_lshlrev_b32_e32 v151, 16, v41
	v_mul_f32_e32 v153, v153, v153
	v_fmac_f32_e32 v153, v151, v151
	v_add_f32_e32 v151, v152, v153
	v_add_f32_e32 v150, v150, v151
	v_add_f32_e32 v149, v150, v149
	ds_read_b128 v[150:153], v141 offset:1536
	ds_read_b128 v[154:157], v141 offset:34560
	s_waitcnt vmcnt(7) lgkmcnt(1)
	v_mfma_f32_16x16x32_bf16 v[2:5], v[34:37], v[150:153], v[2:5]
	v_and_b32_e32 v151, 0xffff0000, v34
	v_lshlrev_b32_e32 v150, 16, v34
	v_and_b32_e32 v153, 0xffff0000, v35
	v_mul_f32_e32 v151, v151, v151
	v_lshlrev_b32_e32 v152, 16, v35
	v_fmac_f32_e32 v151, v150, v150
	v_mul_f32_e32 v150, v153, v153
	s_waitcnt lgkmcnt(0)
	v_mfma_f32_16x16x32_bf16 v[2:5], v[34:37], v[154:157], v[2:5]
	v_and_b32_e32 v155, 0xffff0000, v36
	v_and_b32_e32 v157, 0xffff0000, v37
	v_fmac_f32_e32 v150, v152, v152
	v_lshlrev_b32_e32 v154, 16, v36
	v_lshlrev_b32_e32 v156, 16, v37
	v_add_f32_e32 v150, v151, v150
	v_mul_f32_e32 v151, v155, v155
	v_mul_f32_e32 v152, v157, v157
	v_fmac_f32_e32 v151, v154, v154
	v_fmac_f32_e32 v152, v156, v156
	v_add_f32_e32 v151, v151, v152
	v_add_f32_e32 v150, v150, v151
	v_add_f32_e32 v149, v150, v149
	ds_read_b128 v[150:153], v141 offset:34624
	ds_read_b128 v[154:157], v141 offset:1600
	s_waitcnt vmcnt(6) lgkmcnt(0)
	v_mfma_f32_16x16x32_bf16 v[2:5], v[30:33], v[154:157], v[2:5]
	v_and_b32_e32 v155, 0xffff0000, v32
	v_and_b32_e32 v157, 0xffff0000, v33
	v_lshlrev_b32_e32 v154, 16, v32
	v_mfma_f32_16x16x32_bf16 v[2:5], v[30:33], v[150:153], v[2:5]
	v_and_b32_e32 v151, 0xffff0000, v30
	v_lshlrev_b32_e32 v150, 16, v30
	v_and_b32_e32 v153, 0xffff0000, v31
	v_mul_f32_e32 v151, v151, v151
	v_lshlrev_b32_e32 v152, 16, v31
	v_fmac_f32_e32 v151, v150, v150
	v_mul_f32_e32 v150, v153, v153
	v_fmac_f32_e32 v150, v152, v152
	v_lshlrev_b32_e32 v156, 16, v33
	v_add_f32_e32 v150, v151, v150
	v_mul_f32_e32 v151, v155, v155
	v_mul_f32_e32 v152, v157, v157
	v_fmac_f32_e32 v151, v154, v154
	v_fmac_f32_e32 v152, v156, v156
	v_add_f32_e32 v151, v151, v152
	v_add_f32_e32 v150, v150, v151
	v_add_f32_e32 v149, v150, v149
	ds_read_b128 v[150:153], v141 offset:34688
	ds_read_b128 v[154:157], v141 offset:1664
	s_waitcnt vmcnt(5) lgkmcnt(0)
	v_mfma_f32_16x16x32_bf16 v[2:5], v[26:29], v[154:157], v[2:5]
	v_and_b32_e32 v155, 0xffff0000, v28
	v_and_b32_e32 v157, 0xffff0000, v29
	v_lshlrev_b32_e32 v154, 16, v28
	v_mfma_f32_16x16x32_bf16 v[2:5], v[26:29], v[150:153], v[2:5]
	v_and_b32_e32 v151, 0xffff0000, v26
	v_lshlrev_b32_e32 v150, 16, v26
	v_and_b32_e32 v153, 0xffff0000, v27
	v_mul_f32_e32 v151, v151, v151
	v_lshlrev_b32_e32 v152, 16, v27
	v_fmac_f32_e32 v151, v150, v150
	v_mul_f32_e32 v150, v153, v153
	v_fmac_f32_e32 v150, v152, v152
	v_lshlrev_b32_e32 v156, 16, v29
	v_add_f32_e32 v150, v151, v150
	v_mul_f32_e32 v151, v155, v155
	v_mul_f32_e32 v152, v157, v157
	v_fmac_f32_e32 v151, v154, v154
	v_fmac_f32_e32 v152, v156, v156
	v_add_f32_e32 v151, v151, v152
	v_add_f32_e32 v150, v150, v151
	v_add_f32_e32 v149, v150, v149
	ds_read_b128 v[150:153], v141 offset:34752
	ds_read_b128 v[154:157], v141 offset:1728
	s_waitcnt vmcnt(4) lgkmcnt(0)
	v_mfma_f32_16x16x32_bf16 v[2:5], v[22:25], v[154:157], v[2:5]
	v_mfma_f32_16x16x32_bf16 v[2:5], v[22:25], v[150:153], v[2:5]
	v_and_b32_e32 v151, 0xffff0000, v22
	v_lshlrev_b32_e32 v150, 16, v22
	v_mul_f32_e32 v151, v151, v151
	v_and_b32_e32 v152, 0xffff0000, v23
	v_fmac_f32_e32 v151, v150, v150
	v_lshlrev_b32_e32 v150, 16, v23
	v_mul_f32_e32 v152, v152, v152
	v_fmac_f32_e32 v152, v150, v150
	v_add_f32_e32 v150, v151, v152
	v_and_b32_e32 v152, 0xffff0000, v24
	v_lshlrev_b32_e32 v151, 16, v24
	v_mul_f32_e32 v152, v152, v152
	v_and_b32_e32 v153, 0xffff0000, v25
	v_fmac_f32_e32 v152, v151, v151
	v_lshlrev_b32_e32 v151, 16, v25
	v_mul_f32_e32 v153, v153, v153
	v_fmac_f32_e32 v153, v151, v151
	v_add_f32_e32 v151, v152, v153
	v_add_f32_e32 v150, v150, v151
	v_add_f32_e32 v149, v150, v149
	ds_read_b128 v[150:153], v141 offset:1792
	ds_read_b128 v[154:157], v141 offset:34816
	s_waitcnt vmcnt(3) lgkmcnt(1)
	v_mfma_f32_16x16x32_bf16 v[2:5], v[18:21], v[150:153], v[2:5]
	v_and_b32_e32 v151, 0xffff0000, v18
	v_lshlrev_b32_e32 v150, 16, v18
	v_and_b32_e32 v153, 0xffff0000, v19
	v_mul_f32_e32 v151, v151, v151
	v_lshlrev_b32_e32 v152, 16, v19
	v_fmac_f32_e32 v151, v150, v150
	v_mul_f32_e32 v150, v153, v153
	s_waitcnt lgkmcnt(0)
	v_mfma_f32_16x16x32_bf16 v[2:5], v[18:21], v[154:157], v[2:5]
	v_and_b32_e32 v155, 0xffff0000, v20
	v_and_b32_e32 v157, 0xffff0000, v21
	v_fmac_f32_e32 v150, v152, v152
	v_lshlrev_b32_e32 v154, 16, v20
	v_lshlrev_b32_e32 v156, 16, v21
	v_add_f32_e32 v150, v151, v150
	v_mul_f32_e32 v151, v155, v155
	v_mul_f32_e32 v152, v157, v157
	v_fmac_f32_e32 v151, v154, v154
	v_fmac_f32_e32 v152, v156, v156
	v_add_f32_e32 v151, v151, v152
	v_add_f32_e32 v150, v150, v151
	v_add_f32_e32 v149, v150, v149
	ds_read_b128 v[150:153], v141 offset:34880
	ds_read_b128 v[154:157], v141 offset:1856
	s_waitcnt vmcnt(2) lgkmcnt(0)
	v_mfma_f32_16x16x32_bf16 v[2:5], v[14:17], v[154:157], v[2:5]
	v_and_b32_e32 v155, 0xffff0000, v16
	v_and_b32_e32 v157, 0xffff0000, v17
	v_lshlrev_b32_e32 v154, 16, v16
	v_mfma_f32_16x16x32_bf16 v[2:5], v[14:17], v[150:153], v[2:5]
	v_and_b32_e32 v151, 0xffff0000, v14
	v_lshlrev_b32_e32 v150, 16, v14
	v_and_b32_e32 v153, 0xffff0000, v15
	v_mul_f32_e32 v151, v151, v151
	v_lshlrev_b32_e32 v152, 16, v15
	v_fmac_f32_e32 v151, v150, v150
	v_mul_f32_e32 v150, v153, v153
	v_fmac_f32_e32 v150, v152, v152
	v_lshlrev_b32_e32 v156, 16, v17
	v_add_f32_e32 v150, v151, v150
	v_mul_f32_e32 v151, v155, v155
	v_mul_f32_e32 v152, v157, v157
	v_fmac_f32_e32 v151, v154, v154
	v_fmac_f32_e32 v152, v156, v156
	v_add_f32_e32 v151, v151, v152
	v_add_f32_e32 v150, v150, v151
	v_add_f32_e32 v149, v150, v149
	ds_read_b128 v[150:153], v141 offset:34944
	ds_read_b128 v[154:157], v141 offset:1920
	s_waitcnt vmcnt(1) lgkmcnt(0)
	v_mfma_f32_16x16x32_bf16 v[2:5], v[10:13], v[154:157], v[2:5]
	v_and_b32_e32 v155, 0xffff0000, v12
	v_and_b32_e32 v157, 0xffff0000, v13
	v_lshlrev_b32_e32 v154, 16, v12
	v_mfma_f32_16x16x32_bf16 v[2:5], v[10:13], v[150:153], v[2:5]
	v_and_b32_e32 v151, 0xffff0000, v10
	v_lshlrev_b32_e32 v150, 16, v10
	v_and_b32_e32 v153, 0xffff0000, v11
	v_mul_f32_e32 v151, v151, v151
	v_lshlrev_b32_e32 v152, 16, v11
	v_fmac_f32_e32 v151, v150, v150
	v_mul_f32_e32 v150, v153, v153
	v_fmac_f32_e32 v150, v152, v152
	v_lshlrev_b32_e32 v156, 16, v13
	v_add_f32_e32 v150, v151, v150
	v_mul_f32_e32 v151, v155, v155
	v_mul_f32_e32 v152, v157, v157
	v_fmac_f32_e32 v151, v154, v154
	v_fmac_f32_e32 v152, v156, v156
	v_add_f32_e32 v151, v151, v152
	v_add_f32_e32 v150, v150, v151
	v_add_f32_e32 v149, v150, v149
	ds_read_b128 v[150:153], v141 offset:35008
	ds_read_b128 v[154:157], v141 offset:1984
	s_waitcnt vmcnt(0) lgkmcnt(0)
	v_mfma_f32_16x16x32_bf16 v[2:5], v[6:9], v[154:157], v[2:5]
	v_mfma_f32_16x16x32_bf16 v[2:5], v[6:9], v[150:153], v[2:5]
	v_and_b32_e32 v151, 0xffff0000, v6
	v_lshlrev_b32_e32 v150, 16, v6
	v_mul_f32_e32 v151, v151, v151
	v_and_b32_e32 v152, 0xffff0000, v7
	v_fmac_f32_e32 v151, v150, v150
	v_lshlrev_b32_e32 v150, 16, v7
	v_mul_f32_e32 v152, v152, v152
	v_fmac_f32_e32 v152, v150, v150
	v_add_f32_e32 v150, v151, v152
	v_and_b32_e32 v152, 0xffff0000, v8
	v_lshlrev_b32_e32 v151, 16, v8
	v_mul_f32_e32 v152, v152, v152
	v_and_b32_e32 v153, 0xffff0000, v9
	v_fmac_f32_e32 v152, v151, v151
	v_lshlrev_b32_e32 v151, 16, v9
	v_mul_f32_e32 v153, v153, v153
	v_fmac_f32_e32 v153, v151, v151
	v_add_f32_e32 v151, v152, v153
	v_add_f32_e32 v150, v150, v151
	v_add_f32_e32 v149, v150, v149
	s_nop 0
	v_mov_b32_e32 v150, v149
	s_nop 1
	v_permlane16_swap_b32_e32 v149, v150
	v_add_f32_e32 v149, v149, v150
	v_mov_b32_e32 v150, v149
	s_nop 1
	v_permlane32_swap_b32_e32 v149, v150
	v_add_f32_e32 v149, v149, v150
	v_fmamk_f32 v149, v149, 0x3a800000, v206
	v_cmp_gt_f32_e32 vcc, s72, v149
	v_mul_f32_e32 v150, 0x4f800000, v149
	s_nop 0
	v_cndmask_b32_e32 v149, v149, v150, vcc
	v_sqrt_f32_e32 v150, v149
	s_nop 0
	v_add_u32_e32 v151, -1, v150
	v_fma_f32 v152, -v151, v150, v149
	v_cmp_ge_f32_e64 s[0:1], 0, v152
	v_add_u32_e32 v152, 1, v150
	s_nop 0
	v_cndmask_b32_e64 v151, v150, v151, s[0:1]
	v_fma_f32 v150, -v152, v150, v149
	v_cmp_lt_f32_e64 s[0:1], 0, v150
	s_nop 1
	v_cndmask_b32_e64 v150, v151, v152, s[0:1]
	v_mul_f32_e32 v151, 0x37800000, v150
	v_cndmask_b32_e32 v150, v150, v151, vcc
	v_cmp_class_f32_e32 vcc, v149, v207
	s_nop 1
	v_cndmask_b32_e32 v149, v150, v149, vcc
	v_div_scale_f32 v150, s[0:1], v149, v149, 1.0
	v_rcp_f32_e32 v151, v150
	s_ashr_i32 s0, s6, 6
	s_add_i32 s6, s6, s7
	v_fma_f32 v152, -v150, v151, 1.0
	v_fmac_f32_e32 v151, v152, v151
	v_div_scale_f32 v152, vcc, 1.0, v149, 1.0
	v_mul_f32_e32 v153, v152, v151
	v_fma_f32 v154, -v150, v153, v152
	v_fmac_f32_e32 v153, v154, v151
	v_fma_f32 v150, -v150, v153, v152
	v_div_fmas_f32 v150, v150, v151, v153
	v_div_fixup_f32 v149, v150, v149, 1.0
	v_lshlrev_b32_e32 v150, 16, v130
	v_and_b32_e32 v130, 0xffff0000, v130
	v_mul_f32_e32 v150, v149, v150
	v_mul_f32_e32 v130, v149, v130
	v_mov_b32_e32 v152, v195
	v_cvt_pk_fp8_f32 v152, v150, v130
	v_lshlrev_b32_e32 v151, 16, v131
	v_and_b32_e32 v131, 0xffff0000, v131
	v_mul_f32_e32 v151, v149, v151
	v_mul_f32_e32 v131, v149, v131
	v_cvt_pk_fp8_f32 v152, v151, v131 op_sel:[0,0,1]
	v_lshlrev_b32_e32 v130, 16, v132
	v_and_b32_e32 v131, 0xffff0000, v132
	v_mul_f32_e32 v130, v149, v130
	v_mul_f32_e32 v131, v149, v131
	v_mov_b32_e32 v153, v195
	v_cvt_pk_fp8_f32 v153, v130, v131
	v_lshlrev_b32_e32 v132, 16, v133
	v_and_b32_e32 v133, 0xffff0000, v133
	v_mul_f32_e32 v132, v149, v132
	v_mul_f32_e32 v133, v149, v133
	v_cvt_pk_fp8_f32 v153, v132, v133 op_sel:[0,0,1]
	global_store_dwordx2 v[138:139], v[152:153], off
	s_nop 0
	v_lshlrev_b32_e32 v130, 16, v126
	v_and_b32_e32 v126, 0xffff0000, v126
	v_mul_f32_e32 v131, v149, v126
	v_lshlrev_b32_e32 v126, 16, v127
	v_mul_f32_e32 v132, v149, v126
	v_and_b32_e32 v126, 0xffff0000, v127
	v_mul_f32_e32 v130, v149, v130
	v_mul_f32_e32 v127, v149, v126
	v_mov_b32_e32 v126, v195
	v_cvt_pk_fp8_f32 v126, v130, v131
	v_cvt_pk_fp8_f32 v126, v132, v127 op_sel:[0,0,1]
	v_lshlrev_b32_e32 v127, 16, v128
	v_mul_f32_e32 v130, v149, v127
	v_and_b32_e32 v127, 0xffff0000, v128
	v_mul_f32_e32 v128, v149, v127
	v_lshlrev_b32_e32 v127, 16, v129
	v_mul_f32_e32 v131, v149, v127
	v_and_b32_e32 v127, 0xffff0000, v129
	v_mul_f32_e32 v129, v149, v127
	v_mov_b32_e32 v127, v195
	v_cvt_pk_fp8_f32 v127, v130, v128
	v_cvt_pk_fp8_f32 v127, v131, v129 op_sel:[0,0,1]
	global_store_dwordx2 v[138:139], v[126:127], off offset:32
	s_nop 0
	v_lshlrev_b32_e32 v126, 16, v122
	v_and_b32_e32 v122, 0xffff0000, v122
	v_mul_f32_e32 v127, v149, v122
	v_lshlrev_b32_e32 v122, 16, v123
	v_mul_f32_e32 v128, v149, v122
	v_and_b32_e32 v122, 0xffff0000, v123
	v_mul_f32_e32 v126, v149, v126
	v_mul_f32_e32 v123, v149, v122
	v_mov_b32_e32 v122, v195
	v_cvt_pk_fp8_f32 v122, v126, v127
	v_cvt_pk_fp8_f32 v122, v128, v123 op_sel:[0,0,1]
	v_lshlrev_b32_e32 v123, 16, v124
	v_mul_f32_e32 v126, v149, v123
	v_and_b32_e32 v123, 0xffff0000, v124
	v_mul_f32_e32 v124, v149, v123
	v_lshlrev_b32_e32 v123, 16, v125
	v_mul_f32_e32 v127, v149, v123
	v_and_b32_e32 v123, 0xffff0000, v125
	v_mul_f32_e32 v125, v149, v123
	v_mov_b32_e32 v123, v195
	v_cvt_pk_fp8_f32 v123, v126, v124
	v_cvt_pk_fp8_f32 v123, v127, v125 op_sel:[0,0,1]
	global_store_dwordx2 v[138:139], v[122:123], off offset:64
	s_nop 0
	v_lshlrev_b32_e32 v122, 16, v118
	v_and_b32_e32 v118, 0xffff0000, v118
	v_mul_f32_e32 v123, v149, v118
	v_lshlrev_b32_e32 v118, 16, v119
	v_mul_f32_e32 v124, v149, v118
	v_and_b32_e32 v118, 0xffff0000, v119
	v_mul_f32_e32 v122, v149, v122
	v_mul_f32_e32 v119, v149, v118
	v_mov_b32_e32 v118, v195
	v_cvt_pk_fp8_f32 v118, v122, v123
	v_cvt_pk_fp8_f32 v118, v124, v119 op_sel:[0,0,1]
	v_lshlrev_b32_e32 v119, 16, v120
	v_mul_f32_e32 v122, v149, v119
	v_and_b32_e32 v119, 0xffff0000, v120
	v_mul_f32_e32 v120, v149, v119
	v_lshlrev_b32_e32 v119, 16, v121
	v_mul_f32_e32 v123, v149, v119
	v_and_b32_e32 v119, 0xffff0000, v121
	v_mul_f32_e32 v121, v149, v119
	v_mov_b32_e32 v119, v195
	v_cvt_pk_fp8_f32 v119, v122, v120
	v_cvt_pk_fp8_f32 v119, v123, v121 op_sel:[0,0,1]
	global_store_dwordx2 v[138:139], v[118:119], off offset:96
	s_nop 0
	v_lshlrev_b32_e32 v118, 16, v114
	v_and_b32_e32 v114, 0xffff0000, v114
	v_mul_f32_e32 v119, v149, v114
	v_lshlrev_b32_e32 v114, 16, v115
	v_mul_f32_e32 v120, v149, v114
	v_and_b32_e32 v114, 0xffff0000, v115
	v_mul_f32_e32 v118, v149, v118
	v_mul_f32_e32 v115, v149, v114
	v_mov_b32_e32 v114, v195
	v_cvt_pk_fp8_f32 v114, v118, v119
	v_cvt_pk_fp8_f32 v114, v120, v115 op_sel:[0,0,1]
	v_lshlrev_b32_e32 v115, 16, v116
	v_mul_f32_e32 v118, v149, v115
	v_and_b32_e32 v115, 0xffff0000, v116
	v_mul_f32_e32 v116, v149, v115
	v_lshlrev_b32_e32 v115, 16, v117
	v_mul_f32_e32 v119, v149, v115
	v_and_b32_e32 v115, 0xffff0000, v117
	v_mul_f32_e32 v117, v149, v115
	v_mov_b32_e32 v115, v195
	v_cvt_pk_fp8_f32 v115, v118, v116
	v_cvt_pk_fp8_f32 v115, v119, v117 op_sel:[0,0,1]
	global_store_dwordx2 v[138:139], v[114:115], off offset:128
	s_nop 0
	v_lshlrev_b32_e32 v114, 16, v110
	v_and_b32_e32 v110, 0xffff0000, v110
	v_mul_f32_e32 v115, v149, v110
	v_lshlrev_b32_e32 v110, 16, v111
	v_mul_f32_e32 v116, v149, v110
	v_and_b32_e32 v110, 0xffff0000, v111
	v_mul_f32_e32 v114, v149, v114
	v_mul_f32_e32 v111, v149, v110
	v_mov_b32_e32 v110, v195
	v_cvt_pk_fp8_f32 v110, v114, v115
	v_cvt_pk_fp8_f32 v110, v116, v111 op_sel:[0,0,1]
	v_lshlrev_b32_e32 v111, 16, v112
	v_mul_f32_e32 v114, v149, v111
	v_and_b32_e32 v111, 0xffff0000, v112
	v_mul_f32_e32 v112, v149, v111
	v_lshlrev_b32_e32 v111, 16, v113
	v_mul_f32_e32 v115, v149, v111
	v_and_b32_e32 v111, 0xffff0000, v113
	v_mul_f32_e32 v113, v149, v111
	v_mov_b32_e32 v111, v195
	v_cvt_pk_fp8_f32 v111, v114, v112
	v_cvt_pk_fp8_f32 v111, v115, v113 op_sel:[0,0,1]
	global_store_dwordx2 v[138:139], v[110:111], off offset:160
	s_nop 0
	v_lshlrev_b32_e32 v110, 16, v106
	v_and_b32_e32 v106, 0xffff0000, v106
	v_mul_f32_e32 v111, v149, v106
	v_lshlrev_b32_e32 v106, 16, v107
	v_mul_f32_e32 v112, v149, v106
	v_and_b32_e32 v106, 0xffff0000, v107
	v_mul_f32_e32 v110, v149, v110
	v_mul_f32_e32 v107, v149, v106
	v_mov_b32_e32 v106, v195
	v_cvt_pk_fp8_f32 v106, v110, v111
	v_cvt_pk_fp8_f32 v106, v112, v107 op_sel:[0,0,1]
	v_lshlrev_b32_e32 v107, 16, v108
	v_mul_f32_e32 v110, v149, v107
	v_and_b32_e32 v107, 0xffff0000, v108
	v_mul_f32_e32 v108, v149, v107
	v_lshlrev_b32_e32 v107, 16, v109
	v_mul_f32_e32 v111, v149, v107
	v_and_b32_e32 v107, 0xffff0000, v109
	v_mul_f32_e32 v109, v149, v107
	v_mov_b32_e32 v107, v195
	v_cvt_pk_fp8_f32 v107, v110, v108
	v_cvt_pk_fp8_f32 v107, v111, v109 op_sel:[0,0,1]
	global_store_dwordx2 v[138:139], v[106:107], off offset:192
	s_nop 0
	v_lshlrev_b32_e32 v106, 16, v102
	v_and_b32_e32 v102, 0xffff0000, v102
	v_mul_f32_e32 v107, v149, v102
	v_lshlrev_b32_e32 v102, 16, v103
	v_mul_f32_e32 v108, v149, v102
	v_and_b32_e32 v102, 0xffff0000, v103
	v_mul_f32_e32 v106, v149, v106
	v_mul_f32_e32 v103, v149, v102
	v_mov_b32_e32 v102, v195
	v_cvt_pk_fp8_f32 v102, v106, v107
	v_cvt_pk_fp8_f32 v102, v108, v103 op_sel:[0,0,1]
	v_lshlrev_b32_e32 v103, 16, v104
	v_mul_f32_e32 v106, v149, v103
	v_and_b32_e32 v103, 0xffff0000, v104
	v_mul_f32_e32 v104, v149, v103
	v_lshlrev_b32_e32 v103, 16, v105
	v_mul_f32_e32 v107, v149, v103
	v_and_b32_e32 v103, 0xffff0000, v105
	v_mul_f32_e32 v105, v149, v103
	v_mov_b32_e32 v103, v195
	v_cvt_pk_fp8_f32 v103, v106, v104
	v_cvt_pk_fp8_f32 v103, v107, v105 op_sel:[0,0,1]
	global_store_dwordx2 v[138:139], v[102:103], off offset:224
	s_nop 0
	v_lshlrev_b32_e32 v102, 16, v98
	v_and_b32_e32 v98, 0xffff0000, v98
	v_mul_f32_e32 v103, v149, v98
	v_lshlrev_b32_e32 v98, 16, v99
	v_mul_f32_e32 v104, v149, v98
	v_and_b32_e32 v98, 0xffff0000, v99
	v_mul_f32_e32 v102, v149, v102
	v_mul_f32_e32 v99, v149, v98
	v_mov_b32_e32 v98, v195
	v_cvt_pk_fp8_f32 v98, v102, v103
	v_cvt_pk_fp8_f32 v98, v104, v99 op_sel:[0,0,1]
	v_lshlrev_b32_e32 v99, 16, v100
	v_mul_f32_e32 v102, v149, v99
	v_and_b32_e32 v99, 0xffff0000, v100
	v_mul_f32_e32 v100, v149, v99
	v_lshlrev_b32_e32 v99, 16, v101
	v_mul_f32_e32 v103, v149, v99
	v_and_b32_e32 v99, 0xffff0000, v101
	v_mul_f32_e32 v101, v149, v99
	v_mov_b32_e32 v99, v195
	v_cvt_pk_fp8_f32 v99, v102, v100
	v_cvt_pk_fp8_f32 v99, v103, v101 op_sel:[0,0,1]
	global_store_dwordx2 v[138:139], v[98:99], off offset:256
	s_nop 0
	v_lshlrev_b32_e32 v98, 16, v94
	v_and_b32_e32 v94, 0xffff0000, v94
	v_mul_f32_e32 v99, v149, v94
	v_lshlrev_b32_e32 v94, 16, v95
	v_mul_f32_e32 v100, v149, v94
	v_and_b32_e32 v94, 0xffff0000, v95
	v_mul_f32_e32 v98, v149, v98
	v_mul_f32_e32 v95, v149, v94
	v_mov_b32_e32 v94, v195
	v_cvt_pk_fp8_f32 v94, v98, v99
	v_cvt_pk_fp8_f32 v94, v100, v95 op_sel:[0,0,1]
	v_lshlrev_b32_e32 v95, 16, v96
	v_mul_f32_e32 v98, v149, v95
	v_and_b32_e32 v95, 0xffff0000, v96
	v_mul_f32_e32 v96, v149, v95
	v_lshlrev_b32_e32 v95, 16, v97
	v_mul_f32_e32 v99, v149, v95
	v_and_b32_e32 v95, 0xffff0000, v97
	v_mul_f32_e32 v97, v149, v95
	v_mov_b32_e32 v95, v195
	v_cvt_pk_fp8_f32 v95, v98, v96
	v_cvt_pk_fp8_f32 v95, v99, v97 op_sel:[0,0,1]
	global_store_dwordx2 v[138:139], v[94:95], off offset:288
	s_nop 0
	v_lshlrev_b32_e32 v94, 16, v90
	v_and_b32_e32 v90, 0xffff0000, v90
	v_mul_f32_e32 v95, v149, v90
	v_lshlrev_b32_e32 v90, 16, v91
	v_mul_f32_e32 v96, v149, v90
	v_and_b32_e32 v90, 0xffff0000, v91
	v_mul_f32_e32 v94, v149, v94
	v_mul_f32_e32 v91, v149, v90
	v_mov_b32_e32 v90, v195
	v_cvt_pk_fp8_f32 v90, v94, v95
	v_cvt_pk_fp8_f32 v90, v96, v91 op_sel:[0,0,1]
	v_lshlrev_b32_e32 v91, 16, v92
	v_mul_f32_e32 v94, v149, v91
	v_and_b32_e32 v91, 0xffff0000, v92
	v_mul_f32_e32 v92, v149, v91
	v_lshlrev_b32_e32 v91, 16, v93
	v_mul_f32_e32 v95, v149, v91
	v_and_b32_e32 v91, 0xffff0000, v93
	v_mul_f32_e32 v93, v149, v91
	v_mov_b32_e32 v91, v195
	v_cvt_pk_fp8_f32 v91, v94, v92
	v_cvt_pk_fp8_f32 v91, v95, v93 op_sel:[0,0,1]
	global_store_dwordx2 v[138:139], v[90:91], off offset:320
	s_nop 0
	v_lshlrev_b32_e32 v90, 16, v86
	v_and_b32_e32 v86, 0xffff0000, v86
	v_mul_f32_e32 v91, v149, v86
	v_lshlrev_b32_e32 v86, 16, v87
	v_mul_f32_e32 v92, v149, v86
	v_and_b32_e32 v86, 0xffff0000, v87
	v_mul_f32_e32 v90, v149, v90
	v_mul_f32_e32 v87, v149, v86
	v_mov_b32_e32 v86, v195
	v_cvt_pk_fp8_f32 v86, v90, v91
	v_cvt_pk_fp8_f32 v86, v92, v87 op_sel:[0,0,1]
	v_lshlrev_b32_e32 v87, 16, v88
	v_mul_f32_e32 v90, v149, v87
	v_and_b32_e32 v87, 0xffff0000, v88
	v_mul_f32_e32 v88, v149, v87
	v_lshlrev_b32_e32 v87, 16, v89
	v_mul_f32_e32 v91, v149, v87
	v_and_b32_e32 v87, 0xffff0000, v89
	v_mul_f32_e32 v89, v149, v87
	v_mov_b32_e32 v87, v195
	v_cvt_pk_fp8_f32 v87, v90, v88
	v_cvt_pk_fp8_f32 v87, v91, v89 op_sel:[0,0,1]
	global_store_dwordx2 v[138:139], v[86:87], off offset:352
	s_nop 0
	v_lshlrev_b32_e32 v86, 16, v82
	v_and_b32_e32 v82, 0xffff0000, v82
	v_mul_f32_e32 v87, v149, v82
	v_lshlrev_b32_e32 v82, 16, v83
	v_mul_f32_e32 v88, v149, v82
	v_and_b32_e32 v82, 0xffff0000, v83
	v_mul_f32_e32 v86, v149, v86
	v_mul_f32_e32 v83, v149, v82
	v_mov_b32_e32 v82, v195
	v_cvt_pk_fp8_f32 v82, v86, v87
	v_cvt_pk_fp8_f32 v82, v88, v83 op_sel:[0,0,1]
	v_lshlrev_b32_e32 v83, 16, v84
	v_mul_f32_e32 v86, v149, v83
	v_and_b32_e32 v83, 0xffff0000, v84
	v_mul_f32_e32 v84, v149, v83
	v_lshlrev_b32_e32 v83, 16, v85
	v_mul_f32_e32 v87, v149, v83
	v_and_b32_e32 v83, 0xffff0000, v85
	v_mul_f32_e32 v85, v149, v83
	v_mov_b32_e32 v83, v195
	v_cvt_pk_fp8_f32 v83, v86, v84
	v_cvt_pk_fp8_f32 v83, v87, v85 op_sel:[0,0,1]
	global_store_dwordx2 v[138:139], v[82:83], off offset:384
	s_nop 0
	v_lshlrev_b32_e32 v82, 16, v78
	v_and_b32_e32 v78, 0xffff0000, v78
	v_mul_f32_e32 v83, v149, v78
	v_lshlrev_b32_e32 v78, 16, v79
	v_mul_f32_e32 v84, v149, v78
	v_and_b32_e32 v78, 0xffff0000, v79
	v_mul_f32_e32 v82, v149, v82
	v_mul_f32_e32 v79, v149, v78
	v_mov_b32_e32 v78, v195
	v_cvt_pk_fp8_f32 v78, v82, v83
	v_cvt_pk_fp8_f32 v78, v84, v79 op_sel:[0,0,1]
	v_lshlrev_b32_e32 v79, 16, v80
	v_mul_f32_e32 v82, v149, v79
	v_and_b32_e32 v79, 0xffff0000, v80
	v_mul_f32_e32 v80, v149, v79
	v_lshlrev_b32_e32 v79, 16, v81
	v_mul_f32_e32 v83, v149, v79
	v_and_b32_e32 v79, 0xffff0000, v81
	v_mul_f32_e32 v81, v149, v79
	v_mov_b32_e32 v79, v195
	v_cvt_pk_fp8_f32 v79, v82, v80
	v_cvt_pk_fp8_f32 v79, v83, v81 op_sel:[0,0,1]
	global_store_dwordx2 v[138:139], v[78:79], off offset:416
	s_nop 0
	v_lshlrev_b32_e32 v78, 16, v74
	v_and_b32_e32 v74, 0xffff0000, v74
	v_mul_f32_e32 v79, v149, v74
	v_lshlrev_b32_e32 v74, 16, v75
	v_mul_f32_e32 v80, v149, v74
	v_and_b32_e32 v74, 0xffff0000, v75
	v_mul_f32_e32 v78, v149, v78
	v_mul_f32_e32 v75, v149, v74
	v_mov_b32_e32 v74, v195
	v_cvt_pk_fp8_f32 v74, v78, v79
	v_cvt_pk_fp8_f32 v74, v80, v75 op_sel:[0,0,1]
	v_lshlrev_b32_e32 v75, 16, v76
	v_mul_f32_e32 v78, v149, v75
	v_and_b32_e32 v75, 0xffff0000, v76
	v_mul_f32_e32 v76, v149, v75
	v_lshlrev_b32_e32 v75, 16, v77
	v_mul_f32_e32 v79, v149, v75
	v_and_b32_e32 v75, 0xffff0000, v77
	v_mul_f32_e32 v77, v149, v75
	v_mov_b32_e32 v75, v195
	v_cvt_pk_fp8_f32 v75, v78, v76
	v_cvt_pk_fp8_f32 v75, v79, v77 op_sel:[0,0,1]
	global_store_dwordx2 v[138:139], v[74:75], off offset:448
	s_nop 0
	v_lshlrev_b32_e32 v74, 16, v70
	v_and_b32_e32 v70, 0xffff0000, v70
	v_mul_f32_e32 v75, v149, v70
	v_lshlrev_b32_e32 v70, 16, v71
	v_mul_f32_e32 v76, v149, v70
	v_and_b32_e32 v70, 0xffff0000, v71
	v_mul_f32_e32 v74, v149, v74
	v_mul_f32_e32 v71, v149, v70
	v_mov_b32_e32 v70, v195
	v_cvt_pk_fp8_f32 v70, v74, v75
	v_cvt_pk_fp8_f32 v70, v76, v71 op_sel:[0,0,1]
	v_lshlrev_b32_e32 v71, 16, v72
	v_mul_f32_e32 v74, v149, v71
	v_and_b32_e32 v71, 0xffff0000, v72
	v_mul_f32_e32 v72, v149, v71
	v_lshlrev_b32_e32 v71, 16, v73
	v_mul_f32_e32 v75, v149, v71
	v_and_b32_e32 v71, 0xffff0000, v73
	v_mul_f32_e32 v73, v149, v71
	v_mov_b32_e32 v71, v195
	v_cvt_pk_fp8_f32 v71, v74, v72
	v_cvt_pk_fp8_f32 v71, v75, v73 op_sel:[0,0,1]
	global_store_dwordx2 v[138:139], v[70:71], off offset:480
	s_nop 0
	v_lshlrev_b32_e32 v70, 16, v66
	v_and_b32_e32 v66, 0xffff0000, v66
	v_mul_f32_e32 v71, v149, v66
	v_lshlrev_b32_e32 v66, 16, v67
	v_mul_f32_e32 v72, v149, v66
	v_and_b32_e32 v66, 0xffff0000, v67
	v_mul_f32_e32 v70, v149, v70
	v_mul_f32_e32 v67, v149, v66
	v_mov_b32_e32 v66, v195
	v_cvt_pk_fp8_f32 v66, v70, v71
	v_cvt_pk_fp8_f32 v66, v72, v67 op_sel:[0,0,1]
	v_lshlrev_b32_e32 v67, 16, v68
	v_mul_f32_e32 v70, v149, v67
	v_and_b32_e32 v67, 0xffff0000, v68
	v_mul_f32_e32 v68, v149, v67
	v_lshlrev_b32_e32 v67, 16, v69
	v_mul_f32_e32 v71, v149, v67
	v_and_b32_e32 v67, 0xffff0000, v69
	v_mul_f32_e32 v69, v149, v67
	v_mov_b32_e32 v67, v195
	v_cvt_pk_fp8_f32 v67, v70, v68
	v_cvt_pk_fp8_f32 v67, v71, v69 op_sel:[0,0,1]
	global_store_dwordx2 v[138:139], v[66:67], off offset:512
	s_nop 0
	v_lshlrev_b32_e32 v66, 16, v62
	v_and_b32_e32 v62, 0xffff0000, v62
	v_mul_f32_e32 v67, v149, v62
	v_lshlrev_b32_e32 v62, 16, v63
	v_mul_f32_e32 v68, v149, v62
	v_and_b32_e32 v62, 0xffff0000, v63
	v_mul_f32_e32 v66, v149, v66
	v_mul_f32_e32 v63, v149, v62
	v_mov_b32_e32 v62, v195
	v_cvt_pk_fp8_f32 v62, v66, v67
	v_cvt_pk_fp8_f32 v62, v68, v63 op_sel:[0,0,1]
	v_lshlrev_b32_e32 v63, 16, v64
	v_mul_f32_e32 v66, v149, v63
	v_and_b32_e32 v63, 0xffff0000, v64
	v_mul_f32_e32 v64, v149, v63
	v_lshlrev_b32_e32 v63, 16, v65
	v_mul_f32_e32 v67, v149, v63
	v_and_b32_e32 v63, 0xffff0000, v65
	v_mul_f32_e32 v65, v149, v63
	v_mov_b32_e32 v63, v195
	v_cvt_pk_fp8_f32 v63, v66, v64
	v_cvt_pk_fp8_f32 v63, v67, v65 op_sel:[0,0,1]
	global_store_dwordx2 v[138:139], v[62:63], off offset:544
	s_nop 0
	v_lshlrev_b32_e32 v62, 16, v58
	v_and_b32_e32 v58, 0xffff0000, v58
	v_mul_f32_e32 v63, v149, v58
	v_lshlrev_b32_e32 v58, 16, v59
	v_mul_f32_e32 v64, v149, v58
	v_and_b32_e32 v58, 0xffff0000, v59
	v_mul_f32_e32 v62, v149, v62
	v_mul_f32_e32 v59, v149, v58
	v_mov_b32_e32 v58, v195
	v_cvt_pk_fp8_f32 v58, v62, v63
	v_cvt_pk_fp8_f32 v58, v64, v59 op_sel:[0,0,1]
	v_lshlrev_b32_e32 v59, 16, v60
	v_mul_f32_e32 v62, v149, v59
	v_and_b32_e32 v59, 0xffff0000, v60
	v_mul_f32_e32 v60, v149, v59
	v_lshlrev_b32_e32 v59, 16, v61
	v_mul_f32_e32 v63, v149, v59
	v_and_b32_e32 v59, 0xffff0000, v61
	v_mul_f32_e32 v61, v149, v59
	v_mov_b32_e32 v59, v195
	v_cvt_pk_fp8_f32 v59, v62, v60
	v_cvt_pk_fp8_f32 v59, v63, v61 op_sel:[0,0,1]
	global_store_dwordx2 v[138:139], v[58:59], off offset:576
	s_nop 0
	v_lshlrev_b32_e32 v58, 16, v54
	v_and_b32_e32 v54, 0xffff0000, v54
	v_mul_f32_e32 v59, v149, v54
	v_lshlrev_b32_e32 v54, 16, v55
	v_mul_f32_e32 v60, v149, v54
	v_and_b32_e32 v54, 0xffff0000, v55
	v_mul_f32_e32 v58, v149, v58
	v_mul_f32_e32 v55, v149, v54
	v_mov_b32_e32 v54, v195
	v_cvt_pk_fp8_f32 v54, v58, v59
	v_cvt_pk_fp8_f32 v54, v60, v55 op_sel:[0,0,1]
	v_lshlrev_b32_e32 v55, 16, v56
	v_mul_f32_e32 v58, v149, v55
	v_and_b32_e32 v55, 0xffff0000, v56
	v_mul_f32_e32 v56, v149, v55
	v_lshlrev_b32_e32 v55, 16, v57
	v_mul_f32_e32 v59, v149, v55
	v_and_b32_e32 v55, 0xffff0000, v57
	v_mul_f32_e32 v57, v149, v55
	v_mov_b32_e32 v55, v195
	v_cvt_pk_fp8_f32 v55, v58, v56
	v_cvt_pk_fp8_f32 v55, v59, v57 op_sel:[0,0,1]
	global_store_dwordx2 v[138:139], v[54:55], off offset:608
	s_nop 0
	v_lshlrev_b32_e32 v54, 16, v50
	v_and_b32_e32 v50, 0xffff0000, v50
	v_mul_f32_e32 v55, v149, v50
	v_lshlrev_b32_e32 v50, 16, v51
	v_mul_f32_e32 v56, v149, v50
	v_and_b32_e32 v50, 0xffff0000, v51
	v_mul_f32_e32 v54, v149, v54
	v_mul_f32_e32 v51, v149, v50
	v_mov_b32_e32 v50, v195
	v_cvt_pk_fp8_f32 v50, v54, v55
	v_cvt_pk_fp8_f32 v50, v56, v51 op_sel:[0,0,1]
	v_lshlrev_b32_e32 v51, 16, v52
	v_mul_f32_e32 v54, v149, v51
	v_and_b32_e32 v51, 0xffff0000, v52
	v_mul_f32_e32 v52, v149, v51
	v_lshlrev_b32_e32 v51, 16, v53
	v_mul_f32_e32 v55, v149, v51
	v_and_b32_e32 v51, 0xffff0000, v53
	v_mul_f32_e32 v53, v149, v51
	v_mov_b32_e32 v51, v195
	v_cvt_pk_fp8_f32 v51, v54, v52
	v_cvt_pk_fp8_f32 v51, v55, v53 op_sel:[0,0,1]
	global_store_dwordx2 v[138:139], v[50:51], off offset:640
	s_nop 0
	v_lshlrev_b32_e32 v50, 16, v46
	v_and_b32_e32 v46, 0xffff0000, v46
	v_mul_f32_e32 v51, v149, v46
	v_lshlrev_b32_e32 v46, 16, v47
	v_mul_f32_e32 v52, v149, v46
	v_and_b32_e32 v46, 0xffff0000, v47
	v_mul_f32_e32 v50, v149, v50
	v_mul_f32_e32 v47, v149, v46
	v_mov_b32_e32 v46, v195
	v_cvt_pk_fp8_f32 v46, v50, v51
	v_cvt_pk_fp8_f32 v46, v52, v47 op_sel:[0,0,1]
	v_lshlrev_b32_e32 v47, 16, v48
	v_mul_f32_e32 v50, v149, v47
	v_and_b32_e32 v47, 0xffff0000, v48
	v_mul_f32_e32 v48, v149, v47
	v_lshlrev_b32_e32 v47, 16, v49
	v_mul_f32_e32 v51, v149, v47
	v_and_b32_e32 v47, 0xffff0000, v49
	v_mul_f32_e32 v49, v149, v47
	v_mov_b32_e32 v47, v195
	v_cvt_pk_fp8_f32 v47, v50, v48
	v_cvt_pk_fp8_f32 v47, v51, v49 op_sel:[0,0,1]
	global_store_dwordx2 v[138:139], v[46:47], off offset:672
	s_nop 0
	v_lshlrev_b32_e32 v46, 16, v42
	v_and_b32_e32 v42, 0xffff0000, v42
	v_mul_f32_e32 v47, v149, v42
	v_lshlrev_b32_e32 v42, 16, v43
	v_mul_f32_e32 v48, v149, v42
	v_and_b32_e32 v42, 0xffff0000, v43
	v_mul_f32_e32 v46, v149, v46
	v_mul_f32_e32 v43, v149, v42
	v_mov_b32_e32 v42, v195
	v_cvt_pk_fp8_f32 v42, v46, v47
	v_cvt_pk_fp8_f32 v42, v48, v43 op_sel:[0,0,1]
	v_lshlrev_b32_e32 v43, 16, v44
	v_mul_f32_e32 v46, v149, v43
	v_and_b32_e32 v43, 0xffff0000, v44
	v_mul_f32_e32 v44, v149, v43
	v_lshlrev_b32_e32 v43, 16, v45
	v_mul_f32_e32 v47, v149, v43
	v_and_b32_e32 v43, 0xffff0000, v45
	v_mul_f32_e32 v45, v149, v43
	v_mov_b32_e32 v43, v195
	v_cvt_pk_fp8_f32 v43, v46, v44
	v_cvt_pk_fp8_f32 v43, v47, v45 op_sel:[0,0,1]
	global_store_dwordx2 v[138:139], v[42:43], off offset:704
	s_nop 0
	v_lshlrev_b32_e32 v42, 16, v38
	v_and_b32_e32 v38, 0xffff0000, v38
	v_mul_f32_e32 v43, v149, v38
	v_lshlrev_b32_e32 v38, 16, v39
	v_mul_f32_e32 v44, v149, v38
	v_and_b32_e32 v38, 0xffff0000, v39
	v_mul_f32_e32 v42, v149, v42
	v_mul_f32_e32 v39, v149, v38
	v_mov_b32_e32 v38, v195
	v_cvt_pk_fp8_f32 v38, v42, v43
	v_cvt_pk_fp8_f32 v38, v44, v39 op_sel:[0,0,1]
	v_lshlrev_b32_e32 v39, 16, v40
	v_mul_f32_e32 v42, v149, v39
	v_and_b32_e32 v39, 0xffff0000, v40
	v_mul_f32_e32 v40, v149, v39
	v_lshlrev_b32_e32 v39, 16, v41
	v_mul_f32_e32 v43, v149, v39
	v_and_b32_e32 v39, 0xffff0000, v41
	v_mul_f32_e32 v41, v149, v39
	v_mov_b32_e32 v39, v195
	v_cvt_pk_fp8_f32 v39, v42, v40
	v_cvt_pk_fp8_f32 v39, v43, v41 op_sel:[0,0,1]
	global_store_dwordx2 v[138:139], v[38:39], off offset:736
	s_nop 0
	v_lshlrev_b32_e32 v38, 16, v34
	v_and_b32_e32 v34, 0xffff0000, v34
	v_mul_f32_e32 v39, v149, v34
	v_lshlrev_b32_e32 v34, 16, v35
	v_mul_f32_e32 v40, v149, v34
	v_and_b32_e32 v34, 0xffff0000, v35
	v_mul_f32_e32 v38, v149, v38
	v_mul_f32_e32 v35, v149, v34
	v_mov_b32_e32 v34, v195
	v_cvt_pk_fp8_f32 v34, v38, v39
	v_cvt_pk_fp8_f32 v34, v40, v35 op_sel:[0,0,1]
	v_lshlrev_b32_e32 v35, 16, v36
	v_mul_f32_e32 v38, v149, v35
	v_and_b32_e32 v35, 0xffff0000, v36
	v_mul_f32_e32 v36, v149, v35
	v_lshlrev_b32_e32 v35, 16, v37
	v_mul_f32_e32 v39, v149, v35
	v_and_b32_e32 v35, 0xffff0000, v37
	v_mul_f32_e32 v37, v149, v35
	v_mov_b32_e32 v35, v195
	v_cvt_pk_fp8_f32 v35, v38, v36
	v_cvt_pk_fp8_f32 v35, v39, v37 op_sel:[0,0,1]
	global_store_dwordx2 v[138:139], v[34:35], off offset:768
	s_nop 0
	v_lshlrev_b32_e32 v34, 16, v30
	v_and_b32_e32 v30, 0xffff0000, v30
	v_mul_f32_e32 v35, v149, v30
	v_lshlrev_b32_e32 v30, 16, v31
	v_mul_f32_e32 v36, v149, v30
	v_and_b32_e32 v30, 0xffff0000, v31
	v_mul_f32_e32 v34, v149, v34
	v_mul_f32_e32 v31, v149, v30
	v_mov_b32_e32 v30, v195
	v_cvt_pk_fp8_f32 v30, v34, v35
	v_cvt_pk_fp8_f32 v30, v36, v31 op_sel:[0,0,1]
	v_lshlrev_b32_e32 v31, 16, v32
	v_mul_f32_e32 v34, v149, v31
	v_and_b32_e32 v31, 0xffff0000, v32
	v_mul_f32_e32 v32, v149, v31
	v_lshlrev_b32_e32 v31, 16, v33
	v_mul_f32_e32 v35, v149, v31
	v_and_b32_e32 v31, 0xffff0000, v33
	v_mul_f32_e32 v33, v149, v31
	v_mov_b32_e32 v31, v195
	v_cvt_pk_fp8_f32 v31, v34, v32
	v_cvt_pk_fp8_f32 v31, v35, v33 op_sel:[0,0,1]
	global_store_dwordx2 v[138:139], v[30:31], off offset:800
	s_nop 0
	v_lshlrev_b32_e32 v30, 16, v26
	v_and_b32_e32 v26, 0xffff0000, v26
	v_mul_f32_e32 v31, v149, v26
	v_lshlrev_b32_e32 v26, 16, v27
	v_mul_f32_e32 v32, v149, v26
	v_and_b32_e32 v26, 0xffff0000, v27
	v_mul_f32_e32 v30, v149, v30
	v_mul_f32_e32 v27, v149, v26
	v_mov_b32_e32 v26, v195
	v_cvt_pk_fp8_f32 v26, v30, v31
	v_cvt_pk_fp8_f32 v26, v32, v27 op_sel:[0,0,1]
	v_lshlrev_b32_e32 v27, 16, v28
	v_mul_f32_e32 v30, v149, v27
	v_and_b32_e32 v27, 0xffff0000, v28
	v_mul_f32_e32 v28, v149, v27
	v_lshlrev_b32_e32 v27, 16, v29
	v_mul_f32_e32 v31, v149, v27
	v_and_b32_e32 v27, 0xffff0000, v29
	v_mul_f32_e32 v29, v149, v27
	v_mov_b32_e32 v27, v195
	v_cvt_pk_fp8_f32 v27, v30, v28
	v_cvt_pk_fp8_f32 v27, v31, v29 op_sel:[0,0,1]
	global_store_dwordx2 v[138:139], v[26:27], off offset:832
	s_nop 0
	v_lshlrev_b32_e32 v26, 16, v22
	v_and_b32_e32 v22, 0xffff0000, v22
	v_mul_f32_e32 v27, v149, v22
	v_lshlrev_b32_e32 v22, 16, v23
	v_mul_f32_e32 v28, v149, v22
	v_and_b32_e32 v22, 0xffff0000, v23
	v_mul_f32_e32 v26, v149, v26
	v_mul_f32_e32 v23, v149, v22
	v_mov_b32_e32 v22, v195
	v_cvt_pk_fp8_f32 v22, v26, v27
	v_cvt_pk_fp8_f32 v22, v28, v23 op_sel:[0,0,1]
	v_lshlrev_b32_e32 v23, 16, v24
	v_mul_f32_e32 v26, v149, v23
	v_and_b32_e32 v23, 0xffff0000, v24
	v_mul_f32_e32 v24, v149, v23
	v_lshlrev_b32_e32 v23, 16, v25
	v_mul_f32_e32 v27, v149, v23
	v_and_b32_e32 v23, 0xffff0000, v25
	v_mul_f32_e32 v25, v149, v23
	v_mov_b32_e32 v23, v195
	v_cvt_pk_fp8_f32 v23, v26, v24
	v_cvt_pk_fp8_f32 v23, v27, v25 op_sel:[0,0,1]
	global_store_dwordx2 v[138:139], v[22:23], off offset:864
	s_nop 0
	v_lshlrev_b32_e32 v22, 16, v18
	v_and_b32_e32 v18, 0xffff0000, v18
	v_mul_f32_e32 v23, v149, v18
	v_lshlrev_b32_e32 v18, 16, v19
	v_mul_f32_e32 v24, v149, v18
	v_and_b32_e32 v18, 0xffff0000, v19
	v_mul_f32_e32 v22, v149, v22
	v_mul_f32_e32 v19, v149, v18
	v_mov_b32_e32 v18, v195
	v_cvt_pk_fp8_f32 v18, v22, v23
	v_cvt_pk_fp8_f32 v18, v24, v19 op_sel:[0,0,1]
	v_lshlrev_b32_e32 v19, 16, v20
	v_mul_f32_e32 v22, v149, v19
	v_and_b32_e32 v19, 0xffff0000, v20
	v_mul_f32_e32 v20, v149, v19
	v_lshlrev_b32_e32 v19, 16, v21
	v_mul_f32_e32 v23, v149, v19
	v_and_b32_e32 v19, 0xffff0000, v21
	v_mul_f32_e32 v21, v149, v19
	v_mov_b32_e32 v19, v195
	v_cvt_pk_fp8_f32 v19, v22, v20
	v_cvt_pk_fp8_f32 v19, v23, v21 op_sel:[0,0,1]
	global_store_dwordx2 v[138:139], v[18:19], off offset:896
	s_nop 0
	v_lshlrev_b32_e32 v18, 16, v14
	v_and_b32_e32 v14, 0xffff0000, v14
	v_mul_f32_e32 v19, v149, v14
	v_lshlrev_b32_e32 v14, 16, v15
	v_mul_f32_e32 v20, v149, v14
	v_and_b32_e32 v14, 0xffff0000, v15
	v_mul_f32_e32 v18, v149, v18
	v_mul_f32_e32 v15, v149, v14
	v_mov_b32_e32 v14, v195
	v_cvt_pk_fp8_f32 v14, v18, v19
	v_cvt_pk_fp8_f32 v14, v20, v15 op_sel:[0,0,1]
	v_lshlrev_b32_e32 v15, 16, v16
	v_mul_f32_e32 v18, v149, v15
	v_and_b32_e32 v15, 0xffff0000, v16
	v_mul_f32_e32 v16, v149, v15
	v_lshlrev_b32_e32 v15, 16, v17
	v_mul_f32_e32 v19, v149, v15
	v_and_b32_e32 v15, 0xffff0000, v17
	v_mul_f32_e32 v17, v149, v15
	v_mov_b32_e32 v15, v195
	v_cvt_pk_fp8_f32 v15, v18, v16
	v_cvt_pk_fp8_f32 v15, v19, v17 op_sel:[0,0,1]
	global_store_dwordx2 v[138:139], v[14:15], off offset:928
	s_nop 0
	v_lshlrev_b32_e32 v14, 16, v10
	v_and_b32_e32 v10, 0xffff0000, v10
	v_mul_f32_e32 v15, v149, v10
	v_lshlrev_b32_e32 v10, 16, v11
	v_mul_f32_e32 v16, v149, v10
	v_and_b32_e32 v10, 0xffff0000, v11
	v_mul_f32_e32 v14, v149, v14
	v_mul_f32_e32 v11, v149, v10
	v_mov_b32_e32 v10, v195
	v_cvt_pk_fp8_f32 v10, v14, v15
	v_cvt_pk_fp8_f32 v10, v16, v11 op_sel:[0,0,1]
	v_lshlrev_b32_e32 v11, 16, v12
	v_mul_f32_e32 v14, v149, v11
	v_and_b32_e32 v11, 0xffff0000, v12
	v_mul_f32_e32 v12, v149, v11
	v_lshlrev_b32_e32 v11, 16, v13
	v_mul_f32_e32 v15, v149, v11
	v_and_b32_e32 v11, 0xffff0000, v13
	v_mul_f32_e32 v13, v149, v11
	v_mov_b32_e32 v11, v195
	v_cvt_pk_fp8_f32 v11, v14, v12
	v_cvt_pk_fp8_f32 v11, v15, v13 op_sel:[0,0,1]
	global_store_dwordx2 v[138:139], v[10:11], off offset:960
	s_nop 0
	v_lshlrev_b32_e32 v10, 16, v6
	v_and_b32_e32 v6, 0xffff0000, v6
	v_mul_f32_e32 v11, v149, v6
	v_lshlrev_b32_e32 v6, 16, v7
	v_mul_f32_e32 v12, v149, v6
	v_and_b32_e32 v6, 0xffff0000, v7
	v_mul_f32_e32 v10, v149, v10
	v_mul_f32_e32 v7, v149, v6
	v_mov_b32_e32 v6, v195
	v_cvt_pk_fp8_f32 v6, v10, v11
	v_cvt_pk_fp8_f32 v6, v12, v7 op_sel:[0,0,1]
	v_lshlrev_b32_e32 v7, 16, v8
	v_mul_f32_e32 v10, v149, v7
	v_and_b32_e32 v7, 0xffff0000, v8
	v_mul_f32_e32 v8, v149, v7
	v_lshlrev_b32_e32 v7, 16, v9
	v_mul_f32_e32 v11, v149, v7
	v_and_b32_e32 v7, 0xffff0000, v9
	v_mul_f32_e32 v9, v149, v7
	v_mov_b32_e32 v7, v195
	v_cvt_pk_fp8_f32 v7, v10, v8
	v_add_u32_e32 v8, s8, v142
	s_add_i32 s8, s8, s9
	s_cmpk_lt_i32 s6, 0x800
	v_cvt_pk_fp8_f32 v7, v11, v9 op_sel:[0,0,1]
	ds_bpermute_b32 v9, v143, v149
	global_store_dwordx2 v[138:139], v[6:7], off offset:992
	v_and_or_b32 v6, s0, -16, v140
	s_waitcnt lgkmcnt(0)
	v_mul_f32_e32 v10, v2, v9
	v_ashrrev_i32_e32 v7, 31, v6
	v_lshlrev_b64 v[6:7], 16, v[6:7]
	v_mov_b32_dpp v11, v10 quad_perm:[1,0,3,2] row_mask:0xf bank_mask:0xf bound_ctrl:1
	v_max_f32_e32 v11, v11, v11
	v_max_f32_e32 v10, v10, v11
	v_lshl_add_u64 v[6:7], s[2:3], 0, v[6:7]
	s_nop 0
	v_mov_b32_dpp v11, v10 quad_perm:[2,3,0,1] row_mask:0xf bank_mask:0xf bound_ctrl:1
	v_max_f32_e32 v11, v11, v11
	v_max_f32_e32 v10, v10, v11
	s_nop 1
	v_mov_b32_dpp v11, v10 row_half_mirror row_mask:0xf bank_mask:0xf bound_ctrl:1
	v_max_f32_e32 v11, v11, v11
	v_max_f32_e32 v10, v10, v11
	s_nop 1
	v_mov_b32_dpp v11, v10 row_mirror row_mask:0xf bank_mask:0xf bound_ctrl:1
	v_max_f32_e32 v11, v11, v11
	v_max_f32_e32 v10, v10, v11
	v_fma_f32 v2, v2, v9, -v10
	v_mul_f32_e32 v9, 0x3fb8aa3b, v2
	v_fma_f32 v10, v2, s14, -v9
	v_rndne_f32_e32 v11, v9
	v_fmac_f32_e32 v10, 0x32a5705f, v2
	v_sub_f32_e32 v9, v9, v11
	v_add_f32_e32 v9, v9, v10
	v_exp_f32_e32 v9, v9
	v_cvt_i32_f32_e32 v10, v11
	v_cmp_ngt_f32_e32 vcc, s12, v2
	v_ldexp_f32 v9, v9, v10
	s_nop 0
	v_cndmask_b32_e32 v9, 0, v9, vcc
	v_cmp_nlt_f32_e32 vcc, s13, v2
	v_and_b32_e32 v10, 0x3ffc, v8
	v_lshlrev_b32_e32 v194, 2, v10
	v_cndmask_b32_e32 v2, v252, v9, vcc
	s_nop 1
	v_add_f32_dpp v9, v2, v2 quad_perm:[1,0,3,2] row_mask:0xf bank_mask:0xf bound_ctrl:1
	s_nop 1
	v_add_f32_dpp v9, v9, v9 quad_perm:[2,3,0,1] row_mask:0xf bank_mask:0xf bound_ctrl:1
	s_nop 1
	v_add_f32_dpp v9, v9, v9 row_half_mirror row_mask:0xf bank_mask:0xf bound_ctrl:1
	s_nop 1
	v_add_f32_dpp v9, v9, v9 row_mirror row_mask:0xf bank_mask:0xf bound_ctrl:1
	v_div_scale_f32 v11, s[0:1], v9, v9, v2
	v_rcp_f32_e32 v12, v11
	s_nop 0
	v_fma_f32 v13, -v11, v12, 1.0
	v_fmac_f32_e32 v12, v13, v12
	v_div_scale_f32 v13, vcc, v2, v9, v2
	v_mul_f32_e32 v14, v13, v12
	v_fma_f32 v15, -v11, v14, v13
	v_fmac_f32_e32 v14, v15, v12
	v_fma_f32 v11, -v11, v14, v13
	v_div_fmas_f32 v11, v11, v12, v14
	v_div_fixup_f32 v2, v11, v9, v2
	v_lshl_add_u64 v[10:11], v[6:7], 0, v[194:195]
	global_store_dword v[10:11], v2, off
	ds_bpermute_b32 v2, v144, v149
	v_add_u32_e32 v10, v140, v147
	v_ashrrev_i32_e32 v11, 31, v10
	v_lshl_add_u64 v[10:11], v[10:11], 2, s[4:5]
	global_store_dword v[10:11], v238, off
	s_waitcnt lgkmcnt(0)
	v_mul_f32_e32 v9, v3, v2
	v_add_u32_e32 v147, s10, v147
	s_nop 0
	v_mov_b32_dpp v10, v9 quad_perm:[1,0,3,2] row_mask:0xf bank_mask:0xf bound_ctrl:1
	v_max_f32_e32 v10, v10, v10
	v_max_f32_e32 v9, v9, v10
	s_nop 1
	v_mov_b32_dpp v10, v9 quad_perm:[2,3,0,1] row_mask:0xf bank_mask:0xf bound_ctrl:1
	v_max_f32_e32 v10, v10, v10
	v_max_f32_e32 v9, v9, v10
	s_nop 1
	v_mov_b32_dpp v10, v9 row_half_mirror row_mask:0xf bank_mask:0xf bound_ctrl:1
	v_max_f32_e32 v10, v10, v10
	v_max_f32_e32 v9, v9, v10
	s_nop 1
	v_mov_b32_dpp v10, v9 row_mirror row_mask:0xf bank_mask:0xf bound_ctrl:1
	v_max_f32_e32 v10, v10, v10
	v_max_f32_e32 v9, v9, v10
	v_fma_f32 v2, v3, v2, -v9
	v_mul_f32_e32 v3, 0x3fb8aa3b, v2
	v_fma_f32 v9, v2, s14, -v3
	v_rndne_f32_e32 v10, v3
	v_fmac_f32_e32 v9, 0x32a5705f, v2
	v_sub_f32_e32 v3, v3, v10
	v_add_f32_e32 v3, v3, v9
	v_exp_f32_e32 v3, v3
	v_cvt_i32_f32_e32 v9, v10
	v_cmp_ngt_f32_e32 vcc, s12, v2
	v_ldexp_f32 v3, v3, v9
	s_nop 0
	v_cndmask_b32_e32 v3, 0, v3, vcc
	v_cmp_nlt_f32_e32 vcc, s13, v2
	v_add_u32_e32 v9, 1, v8
	v_and_b32_e32 v9, 0x3ffd, v9
	v_cndmask_b32_e32 v2, v252, v3, vcc
	v_lshlrev_b32_e32 v194, 2, v9
	s_nop 0
	v_add_f32_dpp v3, v2, v2 quad_perm:[1,0,3,2] row_mask:0xf bank_mask:0xf bound_ctrl:1
	s_nop 1
	v_add_f32_dpp v3, v3, v3 quad_perm:[2,3,0,1] row_mask:0xf bank_mask:0xf bound_ctrl:1
	s_nop 1
	v_add_f32_dpp v3, v3, v3 row_half_mirror row_mask:0xf bank_mask:0xf bound_ctrl:1
	s_nop 1
	v_add_f32_dpp v3, v3, v3 row_mirror row_mask:0xf bank_mask:0xf bound_ctrl:1
	v_div_scale_f32 v10, s[0:1], v3, v3, v2
	v_rcp_f32_e32 v11, v10
	s_nop 0
	v_fma_f32 v12, -v10, v11, 1.0
	v_fmac_f32_e32 v11, v12, v11
	v_div_scale_f32 v12, vcc, v2, v3, v2
	v_mul_f32_e32 v13, v12, v11
	v_fma_f32 v14, -v10, v13, v12
	v_fmac_f32_e32 v13, v14, v11
	v_fma_f32 v10, -v10, v13, v12
	v_div_fmas_f32 v10, v10, v11, v13
	v_div_fixup_f32 v10, v10, v3, v2
	v_lshl_add_u64 v[2:3], v[6:7], 0, v[194:195]
	global_store_dword v[2:3], v10, off
	ds_bpermute_b32 v3, v145, v149
	v_add_u32_e32 v2, v140, v148
	v_add_u32_e32 v10, 16, v2
	v_ashrrev_i32_e32 v11, 31, v10
	v_lshl_add_u64 v[10:11], v[10:11], 2, s[4:5]
	s_waitcnt lgkmcnt(0)
	v_mul_f32_e32 v9, v4, v3
	global_store_dword v[10:11], v238, off
	v_add_u32_e32 v148, s10, v148
	v_mov_b32_dpp v10, v9 quad_perm:[1,0,3,2] row_mask:0xf bank_mask:0xf bound_ctrl:1
	v_max_f32_e32 v10, v10, v10
	v_max_f32_e32 v9, v9, v10
	s_nop 1
	v_mov_b32_dpp v10, v9 quad_perm:[2,3,0,1] row_mask:0xf bank_mask:0xf bound_ctrl:1
	v_max_f32_e32 v10, v10, v10
	v_max_f32_e32 v9, v9, v10
	s_nop 1
	v_mov_b32_dpp v10, v9 row_half_mirror row_mask:0xf bank_mask:0xf bound_ctrl:1
	v_max_f32_e32 v10, v10, v10
	v_max_f32_e32 v9, v9, v10
	s_nop 1
	v_mov_b32_dpp v10, v9 row_mirror row_mask:0xf bank_mask:0xf bound_ctrl:1
	v_max_f32_e32 v10, v10, v10
	v_max_f32_e32 v9, v9, v10
	v_fma_f32 v3, v4, v3, -v9
	v_mul_f32_e32 v4, 0x3fb8aa3b, v3
	v_fma_f32 v9, v3, s14, -v4
	v_rndne_f32_e32 v10, v4
	v_fmac_f32_e32 v9, 0x32a5705f, v3
	v_sub_f32_e32 v4, v4, v10
	v_add_f32_e32 v4, v4, v9
	v_exp_f32_e32 v4, v4
	v_cvt_i32_f32_e32 v9, v10
	v_cmp_ngt_f32_e32 vcc, s12, v3
	v_ldexp_f32 v4, v4, v9
	s_nop 0
	v_cndmask_b32_e32 v4, 0, v4, vcc
	v_cmp_nlt_f32_e32 vcc, s13, v3
	v_add_u32_e32 v9, 2, v8
	v_and_b32_e32 v9, 0x3ffe, v9
	v_cndmask_b32_e32 v3, v252, v4, vcc
	v_lshlrev_b32_e32 v194, 2, v9
	s_nop 0
	v_add_f32_dpp v4, v3, v3 quad_perm:[1,0,3,2] row_mask:0xf bank_mask:0xf bound_ctrl:1
	s_nop 1
	v_add_f32_dpp v4, v4, v4 quad_perm:[2,3,0,1] row_mask:0xf bank_mask:0xf bound_ctrl:1
	s_nop 1
	v_add_f32_dpp v4, v4, v4 row_half_mirror row_mask:0xf bank_mask:0xf bound_ctrl:1
	s_nop 1
	v_add_f32_dpp v4, v4, v4 row_mirror row_mask:0xf bank_mask:0xf bound_ctrl:1
	v_div_scale_f32 v10, s[0:1], v4, v4, v3
	v_rcp_f32_e32 v11, v10
	s_nop 0
	v_fma_f32 v12, -v10, v11, 1.0
	v_fmac_f32_e32 v11, v12, v11
	v_div_scale_f32 v12, vcc, v3, v4, v3
	v_mul_f32_e32 v13, v12, v11
	v_fma_f32 v14, -v10, v13, v12
	v_fmac_f32_e32 v13, v14, v11
	v_fma_f32 v10, -v10, v13, v12
	v_div_fmas_f32 v10, v10, v11, v13
	v_div_fixup_f32 v3, v10, v4, v3
	v_lshl_add_u64 v[10:11], v[6:7], 0, v[194:195]
	global_store_dword v[10:11], v3, off
	ds_bpermute_b32 v3, v146, v149
	v_add_u32_e32 v10, 32, v2
	v_ashrrev_i32_e32 v11, 31, v10
	v_lshl_add_u64 v[10:11], v[10:11], 2, s[4:5]
	global_store_dword v[10:11], v238, off
	s_waitcnt lgkmcnt(0)
	v_mul_f32_e32 v4, v5, v3
	v_add_u32_e32 v2, 48, v2
	s_nop 0
	v_mov_b32_dpp v9, v4 quad_perm:[1,0,3,2] row_mask:0xf bank_mask:0xf bound_ctrl:1
	v_max_f32_e32 v9, v9, v9
	v_max_f32_e32 v4, v4, v9
	s_nop 1
	v_mov_b32_dpp v9, v4 quad_perm:[2,3,0,1] row_mask:0xf bank_mask:0xf bound_ctrl:1
	v_max_f32_e32 v9, v9, v9
	v_max_f32_e32 v4, v4, v9
	s_nop 1
	v_mov_b32_dpp v9, v4 row_half_mirror row_mask:0xf bank_mask:0xf bound_ctrl:1
	v_max_f32_e32 v9, v9, v9
	v_max_f32_e32 v4, v4, v9
	s_nop 1
	v_mov_b32_dpp v9, v4 row_mirror row_mask:0xf bank_mask:0xf bound_ctrl:1
	v_max_f32_e32 v9, v9, v9
	v_max_f32_e32 v4, v4, v9
	v_fma_f32 v3, v5, v3, -v4
	v_mul_f32_e32 v4, 0x3fb8aa3b, v3
	v_fma_f32 v5, v3, s14, -v4
	v_rndne_f32_e32 v9, v4
	v_fmac_f32_e32 v5, 0x32a5705f, v3
	v_sub_f32_e32 v4, v4, v9
	v_add_f32_e32 v4, v4, v5
	v_exp_f32_e32 v4, v4
	v_cvt_i32_f32_e32 v5, v9
	v_cmp_ngt_f32_e32 vcc, s12, v3
	v_ldexp_f32 v4, v4, v5
	s_nop 0
	v_cndmask_b32_e32 v4, 0, v4, vcc
	v_cmp_nlt_f32_e32 vcc, s13, v3
	v_add_u32_e32 v5, 3, v8
	v_and_b32_e32 v5, 0x3fff, v5
	v_cndmask_b32_e32 v3, v252, v4, vcc
	v_lshlrev_b32_e32 v194, 2, v5
	s_nop 0
	v_add_f32_dpp v4, v3, v3 quad_perm:[1,0,3,2] row_mask:0xf bank_mask:0xf bound_ctrl:1
	s_nop 1
	v_add_f32_dpp v4, v4, v4 quad_perm:[2,3,0,1] row_mask:0xf bank_mask:0xf bound_ctrl:1
	s_nop 1
	v_add_f32_dpp v4, v4, v4 row_half_mirror row_mask:0xf bank_mask:0xf bound_ctrl:1
	s_nop 1
	v_add_f32_dpp v4, v4, v4 row_mirror row_mask:0xf bank_mask:0xf bound_ctrl:1
	v_div_scale_f32 v8, s[0:1], v4, v4, v3
	v_rcp_f32_e32 v9, v8
	s_nop 0
	v_fma_f32 v10, -v8, v9, 1.0
	v_fmac_f32_e32 v9, v10, v9
	v_div_scale_f32 v10, vcc, v3, v4, v3
	v_mul_f32_e32 v11, v10, v9
	v_fma_f32 v12, -v8, v11, v10
	v_fmac_f32_e32 v11, v12, v9
	v_fma_f32 v8, -v8, v11, v10
	v_div_fmas_f32 v8, v8, v9, v11
	v_div_fixup_f32 v3, v8, v4, v3
	v_lshl_add_u64 v[4:5], v[6:7], 0, v[194:195]
	global_store_dword v[4:5], v3, off
	v_ashrrev_i32_e32 v3, 31, v2
	v_lshl_add_u64 v[2:3], v[2:3], 2, s[4:5]
	global_store_dword v[2:3], v238, off
	s_cbranch_scc1 .LBB0_731
	s_mov_b32 s96, 0x3fb8aa3b

.LBB0_957:
	s_cmp_eq_u32 s58, s55
	s_cselect_b64 s[22:23], -1, 0
	s_or_b64 s[26:27], s[4:5], s[22:23]
	s_and_b64 vcc, exec, s[26:27]
	s_cbranch_vccnz .LBB0_959
	s_lshl_b32 s19, s58, 8
	v_lshrrev_b32_e32 v2, 7, v0
	v_bfe_u32 v3, v0, 2, 4
	v_lshl_add_u32 v2, v2, 4, v3
	v_add_u32_e32 v2, s19, v2
	v_mov_b32_e32 v3, 0
	v_lshl_add_u64 v[4:5], v[2:3], 2, s[8:9]
	global_load_dword v172, v[4:5], off
	global_load_dword v173, v[4:5], off offset:512
	global_load_dword v174, v[4:5], off offset:256
	global_load_dword v175, v[4:5], off offset:768
